# GEMM K-loops (proj, out, MoE1, MoE2, MoE2 half-N): 8-byte and 16-byte instructions placed on 8-byte boundaries
# baseline (speedup 1.0000x reference)
.LBB0_496:
	v_mov_b32_e32 v64, 0
	v_mov_b32_e32 v209, v97
	v_mov_b32_e32 v211, v97
	s_mov_b32 s5, 0
	s_mov_b64 s[26:27], 0
	v_mov_b32_e32 v65, v64
	v_mov_b32_e32 v66, v64
	v_mov_b32_e32 v67, v64
	v_mov_b32_e32 v68, v64
	v_mov_b32_e32 v69, v64
	v_mov_b32_e32 v70, v64
	v_mov_b32_e32 v71, v64
	v_mov_b32_e32 v80, v64
	v_mov_b32_e32 v81, v64
	v_mov_b32_e32 v82, v64
	v_mov_b32_e32 v83, v64
	v_mov_b32_e32 v84, v64
	v_mov_b32_e32 v85, v64
	v_mov_b32_e32 v86, v64
	v_mov_b32_e32 v87, v64
	v_mov_b32_e32 v98, v64
	v_mov_b32_e32 v99, v64
	v_mov_b32_e32 v100, v64
	v_mov_b32_e32 v101, v64
	v_mov_b32_e32 v102, v64
	v_mov_b32_e32 v103, v64
	v_mov_b32_e32 v104, v64
	v_mov_b32_e32 v105, v64
	v_mov_b32_e32 v114, v64
	v_mov_b32_e32 v115, v64
	v_mov_b32_e32 v116, v64
	v_mov_b32_e32 v117, v64
	v_mov_b32_e32 v118, v64
	v_mov_b32_e32 v119, v64
	v_mov_b32_e32 v120, v64
	v_mov_b32_e32 v121, v64
	v_mov_b32_e32 v72, v64
	v_mov_b32_e32 v73, v64
	v_mov_b32_e32 v74, v64
	v_mov_b32_e32 v75, v64
	v_mov_b32_e32 v76, v64
	v_mov_b32_e32 v77, v64
	v_mov_b32_e32 v78, v64
	v_mov_b32_e32 v79, v64
	v_mov_b32_e32 v88, v64
	v_mov_b32_e32 v89, v64
	v_mov_b32_e32 v90, v64
	v_mov_b32_e32 v91, v64
	v_mov_b32_e32 v92, v64
	v_mov_b32_e32 v93, v64
	v_mov_b32_e32 v94, v64
	v_mov_b32_e32 v95, v64
	v_mov_b32_e32 v106, v64
	v_mov_b32_e32 v107, v64
	v_mov_b32_e32 v108, v64
	v_mov_b32_e32 v109, v64
	v_mov_b32_e32 v110, v64
	v_mov_b32_e32 v111, v64
	v_mov_b32_e32 v112, v64
	v_mov_b32_e32 v113, v64
	v_mov_b32_e32 v122, v64
	v_mov_b32_e32 v123, v64
	v_mov_b32_e32 v124, v64
	v_mov_b32_e32 v125, v64
	v_mov_b32_e32 v126, v64
	v_mov_b32_e32 v127, v64
	v_mov_b32_e32 v128, v64
	v_mov_b32_e32 v129, v64
	v_mov_b32_e32 v130, v64
	v_mov_b32_e32 v131, v64
	v_mov_b32_e32 v132, v64
	v_mov_b32_e32 v133, v64
	v_mov_b32_e32 v134, v64
	v_mov_b32_e32 v135, v64
	v_mov_b32_e32 v136, v64
	v_mov_b32_e32 v137, v64
	v_mov_b32_e32 v146, v64
	v_mov_b32_e32 v147, v64
	v_mov_b32_e32 v148, v64
	v_mov_b32_e32 v149, v64
	v_mov_b32_e32 v150, v64
	v_mov_b32_e32 v151, v64
	v_mov_b32_e32 v152, v64
	v_mov_b32_e32 v153, v64
	v_mov_b32_e32 v162, v64
	v_mov_b32_e32 v163, v64
	v_mov_b32_e32 v164, v64
	v_mov_b32_e32 v165, v64
	v_mov_b32_e32 v166, v64
	v_mov_b32_e32 v167, v64
	v_mov_b32_e32 v168, v64
	v_mov_b32_e32 v169, v64
	v_mov_b32_e32 v178, v64
	v_mov_b32_e32 v179, v64
	v_mov_b32_e32 v180, v64
	v_mov_b32_e32 v181, v64
	v_mov_b32_e32 v182, v64
	v_mov_b32_e32 v183, v64
	v_mov_b32_e32 v184, v64
	v_mov_b32_e32 v185, v64
	v_mov_b32_e32 v138, v64
	v_mov_b32_e32 v139, v64
	v_mov_b32_e32 v140, v64
	v_mov_b32_e32 v141, v64
	v_mov_b32_e32 v142, v64
	v_mov_b32_e32 v143, v64
	v_mov_b32_e32 v144, v64
	v_mov_b32_e32 v145, v64
	v_mov_b32_e32 v154, v64
	v_mov_b32_e32 v155, v64
	v_mov_b32_e32 v156, v64
	v_mov_b32_e32 v157, v64
	v_mov_b32_e32 v158, v64
	v_mov_b32_e32 v159, v64
	v_mov_b32_e32 v160, v64
	v_mov_b32_e32 v161, v64
	v_mov_b32_e32 v170, v64
	v_mov_b32_e32 v171, v64
	v_mov_b32_e32 v172, v64
	v_mov_b32_e32 v173, v64
	v_mov_b32_e32 v174, v64
	v_mov_b32_e32 v175, v64
	v_mov_b32_e32 v176, v64
	v_mov_b32_e32 v177, v64
	v_mov_b32_e32 v186, v64
	v_mov_b32_e32 v187, v64
	v_mov_b32_e32 v188, v64
	v_mov_b32_e32 v189, v64
	v_mov_b32_e32 v190, v64
	v_mov_b32_e32 v191, v64
	v_mov_b32_e32 v192, v64
	v_mov_b32_e32 v193, v64
	s_nop 0
.LBB0_497:
	s_cmpk_eq_i32 s26, 0x300
	s_cselect_b64 s[28:29], -1, 0
	s_add_i32 s23, 0, 0x10000
	s_add_i32 s30, 0, 0x14000
	ds_read_b128 v[8:11], v205
	ds_read_b128 v[12:15], v237
	ds_read_b128 v[24:27], v205 offset:2048
	ds_read_b128 v[28:31], v237 offset:2048
	ds_read_b128 v[0:3], v205 offset:16384
	ds_read_b128 v[4:7], v237 offset:16384
	ds_read_b128 v[16:19], v205 offset:18432
	ds_read_b128 v[20:23], v237 offset:18432
	s_add_i32 m0, s49, 0xc000
	s_add_u32 s30, s46, s26
	s_addc_u32 s31, s9, s27
	s_add_i32 s23, s49, 0xe000
	s_cmpk_lg_i32 s26, 0x300
	s_nop 0
	ds_read_b128 v[40:43], v239
	ds_read_b128 v[32:35], v239 offset:2048
	ds_read_b128 v[44:47], v240
	ds_read_b128 v[36:39], v240 offset:2048
	ds_read_b128 v[56:59], v239 offset:4096
	ds_read_b128 v[48:51], v239 offset:6144
	ds_read_b128 v[60:63], v240 offset:4096
	ds_read_b128 v[52:55], v240 offset:6144
	global_load_lds_dwordx4 v96, s[30:31]
	s_mov_b32 m0, s23
	s_nop 0
	global_load_lds_dwordx4 v206, s[30:31]
	s_waitcnt vmcnt(8)
	s_waitcnt lgkmcnt(0)
	s_barrier
	s_setprio 1
	s_waitcnt lgkmcnt(0)
	s_nop 0
	v_mfma_scale_f32_16x16x128_f8f6f4 v[190:193], v[8:15], v[40:47], v[190:193], v226, v225 op_sel_hi:[0,0,0]
	v_mfma_scale_f32_16x16x128_f8f6f4 v[186:189], v[24:31], v[40:47], v[186:189], v226, v225 op_sel_hi:[0,0,0]
	v_mfma_scale_f32_16x16x128_f8f6f4 v[174:177], v[8:15], v[32:39], v[174:177], v226, v225 op_sel_hi:[0,0,0]
	v_mfma_scale_f32_16x16x128_f8f6f4 v[170:173], v[24:31], v[32:39], v[170:173], v226, v225 op_sel_hi:[0,0,0]
	v_mfma_scale_f32_16x16x128_f8f6f4 v[158:161], v[8:15], v[56:63], v[158:161], v226, v225 op_sel_hi:[0,0,0]
	v_mfma_scale_f32_16x16x128_f8f6f4 v[154:157], v[24:31], v[56:63], v[154:157], v226, v225 op_sel_hi:[0,0,0]
	v_mfma_scale_f32_16x16x128_f8f6f4 v[142:145], v[8:15], v[48:55], v[142:145], v226, v225 op_sel_hi:[0,0,0]
	v_mfma_scale_f32_16x16x128_f8f6f4 v[138:141], v[24:31], v[48:55], v[138:141], v226, v225 op_sel_hi:[0,0,0]
	s_setprio 0
	s_setprio 1
	v_mfma_scale_f32_16x16x128_f8f6f4 v[182:185], v[0:7], v[40:47], v[182:185], v226, v225 op_sel_hi:[0,0,0]
	v_mfma_scale_f32_16x16x128_f8f6f4 v[178:181], v[16:23], v[40:47], v[178:181], v226, v225 op_sel_hi:[0,0,0]
	v_mfma_scale_f32_16x16x128_f8f6f4 v[166:169], v[0:7], v[32:39], v[166:169], v226, v225 op_sel_hi:[0,0,0]
	v_mfma_scale_f32_16x16x128_f8f6f4 v[162:165], v[16:23], v[32:39], v[162:165], v226, v225 op_sel_hi:[0,0,0]
	v_mfma_scale_f32_16x16x128_f8f6f4 v[150:153], v[0:7], v[56:63], v[150:153], v226, v225 op_sel_hi:[0,0,0]
	v_mfma_scale_f32_16x16x128_f8f6f4 v[146:149], v[16:23], v[56:63], v[146:149], v226, v225 op_sel_hi:[0,0,0]
	v_mfma_scale_f32_16x16x128_f8f6f4 v[134:137], v[0:7], v[48:55], v[134:137], v226, v225 op_sel_hi:[0,0,0]
	v_mfma_scale_f32_16x16x128_f8f6f4 v[130:133], v[16:23], v[48:55], v[130:133], v226, v225 op_sel_hi:[0,0,0]
	s_setprio 0
	s_barrier
	s_cbranch_scc1 .LBB0_499
	v_mov_b64_e32 v[212:213], v[210:211]
	v_mov_b64_e32 v[214:215], v[208:209]
	v_mov_b32_e32 v206, v210
	v_mov_b32_e32 v96, v208
	v_mov_b32_e32 v204, v243
	v_mov_b32_e32 v202, v224
	v_mov_b32_e32 v241, v210
	v_mov_b32_e32 v242, v208
	s_branch .LBB0_500
.LBB0_499:
	v_mov_b32_e64 v207, v97
	v_mov_b64_e32 v[212:213], v[206:207]
	v_mov_b64_e32 v[214:215], v[96:97]
.LBB0_500:
	s_and_b64 s[30:31], s[24:25], s[28:29]
	s_add_i32 s23, s5, 2
	s_and_b64 s[28:29], s[28:29], exec
	s_cselect_b32 s96, 0, s23
	s_and_b64 s[28:29], s[30:31], exec
	s_cselect_b32 s28, s52, s4
	s_ashr_i32 s29, s28, 31
	s_lshl_b64 s[30:31], s[96:97], 7
	s_or_b32 s96, s96, 1
	s_lshl_b64 s[34:35], s[28:29], 18
	s_lshl_b64 s[28:29], s[96:97], 7
	s_add_u32 s72, s6, s34
	s_addc_u32 s73, s7, s35
	s_add_u32 s34, s72, s30
	s_addc_u32 s35, s73, s31
	s_mov_b32 m0, s56
	ds_read_b128 v[56:59], v239 offset:16384
	ds_read_b128 v[60:63], v240 offset:16384
	ds_read_b128 v[48:51], v239 offset:18432
	ds_read_b128 v[52:55], v240 offset:18432
	ds_read_b128 v[40:43], v239 offset:20480
	ds_read_b128 v[44:47], v240 offset:20480
	ds_read_b128 v[32:35], v239 offset:22528
	ds_read_b128 v[36:39], v240 offset:22528
	global_load_lds_dwordx4 v194, s[34:35]
	s_mov_b32 m0, s57
	s_nop 0
	global_load_lds_dwordx4 v196, s[34:35]
	s_add_u32 s34, s34, 0x20000
	s_addc_u32 s35, s35, 0
	s_mov_b32 m0, s58
	s_add_u32 s30, s78, s30
	s_nop 0
	global_load_lds_dwordx4 v194, s[34:35]
	s_mov_b32 m0, s59
	s_addc_u32 s31, s79, s31
	global_load_lds_dwordx4 v196, s[34:35]
	s_mov_b32 m0, s49
	s_nop 0
	global_load_lds_dwordx4 v202, s[30:31]
	s_mov_b32 m0, s60
	s_nop 0
	global_load_lds_dwordx4 v204, s[30:31]
	s_waitcnt vmcnt(8)
	s_waitcnt lgkmcnt(0)
	s_barrier
	s_setprio 1
	s_waitcnt lgkmcnt(0)
	s_nop 0
	v_mfma_scale_f32_16x16x128_f8f6f4 v[126:129], v[8:15], v[56:63], v[126:129], v226, v225 op_sel_hi:[0,0,0]
	v_mfma_scale_f32_16x16x128_f8f6f4 v[122:125], v[24:31], v[56:63], v[122:125], v226, v225 op_sel_hi:[0,0,0]
	v_mfma_scale_f32_16x16x128_f8f6f4 v[110:113], v[8:15], v[48:55], v[110:113], v226, v225 op_sel_hi:[0,0,0]
	v_mfma_scale_f32_16x16x128_f8f6f4 v[106:109], v[24:31], v[48:55], v[106:109], v226, v225 op_sel_hi:[0,0,0]
	v_mfma_scale_f32_16x16x128_f8f6f4 v[92:95], v[8:15], v[40:47], v[92:95], v226, v225 op_sel_hi:[0,0,0]
	v_mfma_scale_f32_16x16x128_f8f6f4 v[88:91], v[24:31], v[40:47], v[88:91], v226, v225 op_sel_hi:[0,0,0]
	v_mfma_scale_f32_16x16x128_f8f6f4 v[76:79], v[8:15], v[32:39], v[76:79], v226, v225 op_sel_hi:[0,0,0]
	v_mfma_scale_f32_16x16x128_f8f6f4 v[72:75], v[24:31], v[32:39], v[72:75], v226, v225 op_sel_hi:[0,0,0]
	s_setprio 0
	s_setprio 1
	v_mfma_scale_f32_16x16x128_f8f6f4 v[118:121], v[0:7], v[56:63], v[118:121], v226, v225 op_sel_hi:[0,0,0]
	v_mfma_scale_f32_16x16x128_f8f6f4 v[114:117], v[16:23], v[56:63], v[114:117], v226, v225 op_sel_hi:[0,0,0]
	v_mfma_scale_f32_16x16x128_f8f6f4 v[102:105], v[0:7], v[48:55], v[102:105], v226, v225 op_sel_hi:[0,0,0]
	v_mfma_scale_f32_16x16x128_f8f6f4 v[98:101], v[16:23], v[48:55], v[98:101], v226, v225 op_sel_hi:[0,0,0]
	v_mfma_scale_f32_16x16x128_f8f6f4 v[84:87], v[0:7], v[40:47], v[84:87], v226, v225 op_sel_hi:[0,0,0]
	v_mfma_scale_f32_16x16x128_f8f6f4 v[80:83], v[16:23], v[40:47], v[80:83], v226, v225 op_sel_hi:[0,0,0]
	v_mfma_scale_f32_16x16x128_f8f6f4 v[68:71], v[0:7], v[32:39], v[68:71], v226, v225 op_sel_hi:[0,0,0]
	v_mfma_scale_f32_16x16x128_f8f6f4 v[64:67], v[16:23], v[32:39], v[64:67], v226, v225 op_sel_hi:[0,0,0]
	s_setprio 0
	s_barrier
	s_add_i32 s34, 0, 0x18000
	s_add_i32 s35, 0, 0x1c000
	ds_read_b128 v[0:3], v205 offset:32768
	ds_read_b128 v[4:7], v237 offset:32768
	ds_read_b128 v[8:11], v205 offset:34816
	ds_read_b128 v[12:15], v237 offset:34816
	ds_read_b128 v[16:19], v205 offset:49152
	ds_read_b128 v[20:23], v237 offset:49152
	ds_read_b128 v[24:27], v205 offset:51200
	ds_read_b128 v[28:31], v237 offset:51200
	s_mov_b32 m0, s61
	s_nop 0
	ds_read_b128 v[32:35], v239 offset:32768
	ds_read_b128 v[40:43], v239 offset:34816
	ds_read_b128 v[36:39], v240 offset:32768
	ds_read_b128 v[44:47], v240 offset:34816
	ds_read_b128 v[48:51], v239 offset:36864
	ds_read_b128 v[56:59], v239 offset:38912
	ds_read_b128 v[52:55], v240 offset:36864
	ds_read_b128 v[60:63], v240 offset:38912
	global_load_lds_dwordx4 v214, s[30:31]
	s_mov_b32 m0, s64
	s_nop 0
	global_load_lds_dwordx4 v212, s[30:31]
	s_waitcnt vmcnt(8)
	s_waitcnt lgkmcnt(0)
	s_barrier
	s_setprio 1
	s_waitcnt lgkmcnt(0)
	s_nop 0
	v_mfma_scale_f32_16x16x128_f8f6f4 v[190:193], v[0:7], v[32:39], v[190:193], v226, v225 op_sel_hi:[0,0,0]
	v_mfma_scale_f32_16x16x128_f8f6f4 v[186:189], v[8:15], v[32:39], v[186:189], v226, v225 op_sel_hi:[0,0,0]
	v_mfma_scale_f32_16x16x128_f8f6f4 v[174:177], v[0:7], v[40:47], v[174:177], v226, v225 op_sel_hi:[0,0,0]
	v_mfma_scale_f32_16x16x128_f8f6f4 v[170:173], v[8:15], v[40:47], v[170:173], v226, v225 op_sel_hi:[0,0,0]
	v_mfma_scale_f32_16x16x128_f8f6f4 v[158:161], v[0:7], v[48:55], v[158:161], v226, v225 op_sel_hi:[0,0,0]
	v_mfma_scale_f32_16x16x128_f8f6f4 v[154:157], v[8:15], v[48:55], v[154:157], v226, v225 op_sel_hi:[0,0,0]
	v_mfma_scale_f32_16x16x128_f8f6f4 v[142:145], v[0:7], v[56:63], v[142:145], v226, v225 op_sel_hi:[0,0,0]
	v_mfma_scale_f32_16x16x128_f8f6f4 v[138:141], v[8:15], v[56:63], v[138:141], v226, v225 op_sel_hi:[0,0,0]
	s_setprio 0
	s_setprio 1
	v_mfma_scale_f32_16x16x128_f8f6f4 v[182:185], v[16:23], v[32:39], v[182:185], v226, v225 op_sel_hi:[0,0,0]
	v_mfma_scale_f32_16x16x128_f8f6f4 v[178:181], v[24:31], v[32:39], v[178:181], v226, v225 op_sel_hi:[0,0,0]
	v_mfma_scale_f32_16x16x128_f8f6f4 v[166:169], v[16:23], v[40:47], v[166:169], v226, v225 op_sel_hi:[0,0,0]
	v_mfma_scale_f32_16x16x128_f8f6f4 v[162:165], v[24:31], v[40:47], v[162:165], v226, v225 op_sel_hi:[0,0,0]
	v_mfma_scale_f32_16x16x128_f8f6f4 v[150:153], v[16:23], v[48:55], v[150:153], v226, v225 op_sel_hi:[0,0,0]
	v_mfma_scale_f32_16x16x128_f8f6f4 v[146:149], v[24:31], v[48:55], v[146:149], v226, v225 op_sel_hi:[0,0,0]
	v_mfma_scale_f32_16x16x128_f8f6f4 v[134:137], v[16:23], v[56:63], v[134:137], v226, v225 op_sel_hi:[0,0,0]
	v_mfma_scale_f32_16x16x128_f8f6f4 v[130:133], v[24:31], v[56:63], v[130:133], v226, v225 op_sel_hi:[0,0,0]
	s_setprio 0
	s_barrier
	s_add_u32 s30, s72, s28
	s_addc_u32 s31, s73, s29
	s_add_i32 s34, s34, s48
	s_mov_b32 m0, s34
	ds_read_b128 v[32:35], v239 offset:49152
	ds_read_b128 v[40:43], v239 offset:51200
	ds_read_b128 v[36:39], v240 offset:49152
	ds_read_b128 v[44:47], v240 offset:51200
	ds_read_b128 v[48:51], v239 offset:53248
	ds_read_b128 v[56:59], v239 offset:55296
	ds_read_b128 v[52:55], v240 offset:53248
	ds_read_b128 v[60:63], v240 offset:55296
	global_load_lds_dwordx4 v194, s[30:31]
	s_add_i32 m0, s34, 0x2000
	s_add_i32 s34, s35, s48
	s_nop 0
	global_load_lds_dwordx4 v196, s[30:31]
	s_add_u32 s30, s30, 0x20000
	s_addc_u32 s31, s31, 0
	s_mov_b32 m0, s34
	s_nop 0
	s_nop 0
	global_load_lds_dwordx4 v194, s[30:31]
	s_add_i32 m0, s34, 0x2000
	s_add_u32 s28, s78, s28
	s_nop 0
	global_load_lds_dwordx4 v196, s[30:31]
	s_addc_u32 s29, s79, s29
	s_mov_b32 m0, s65
	s_nop 0
	s_nop 0
	global_load_lds_dwordx4 v202, s[28:29]
	s_mov_b32 m0, s92
	s_nop 0
	global_load_lds_dwordx4 v204, s[28:29]
	s_waitcnt vmcnt(8)
	s_waitcnt lgkmcnt(0)
	s_barrier
	s_setprio 1
	s_waitcnt lgkmcnt(0)
	s_nop 0
	v_mfma_scale_f32_16x16x128_f8f6f4 v[126:129], v[0:7], v[32:39], v[126:129], v226, v225 op_sel_hi:[0,0,0]
	v_mfma_scale_f32_16x16x128_f8f6f4 v[122:125], v[8:15], v[32:39], v[122:125], v226, v225 op_sel_hi:[0,0,0]
	v_mfma_scale_f32_16x16x128_f8f6f4 v[110:113], v[0:7], v[40:47], v[110:113], v226, v225 op_sel_hi:[0,0,0]
	v_mfma_scale_f32_16x16x128_f8f6f4 v[106:109], v[8:15], v[40:47], v[106:109], v226, v225 op_sel_hi:[0,0,0]
	v_mfma_scale_f32_16x16x128_f8f6f4 v[92:95], v[0:7], v[48:55], v[92:95], v226, v225 op_sel_hi:[0,0,0]
	v_mfma_scale_f32_16x16x128_f8f6f4 v[88:91], v[8:15], v[48:55], v[88:91], v226, v225 op_sel_hi:[0,0,0]
	v_mfma_scale_f32_16x16x128_f8f6f4 v[76:79], v[0:7], v[56:63], v[76:79], v226, v225 op_sel_hi:[0,0,0]
	v_mfma_scale_f32_16x16x128_f8f6f4 v[72:75], v[8:15], v[56:63], v[72:75], v226, v225 op_sel_hi:[0,0,0]
	s_setprio 0
	s_setprio 1
	v_mfma_scale_f32_16x16x128_f8f6f4 v[118:121], v[16:23], v[32:39], v[118:121], v226, v225 op_sel_hi:[0,0,0]
	v_mfma_scale_f32_16x16x128_f8f6f4 v[114:117], v[24:31], v[32:39], v[114:117], v226, v225 op_sel_hi:[0,0,0]
	v_mfma_scale_f32_16x16x128_f8f6f4 v[102:105], v[16:23], v[40:47], v[102:105], v226, v225 op_sel_hi:[0,0,0]
	v_mfma_scale_f32_16x16x128_f8f6f4 v[98:101], v[24:31], v[40:47], v[98:101], v226, v225 op_sel_hi:[0,0,0]
	v_mfma_scale_f32_16x16x128_f8f6f4 v[84:87], v[16:23], v[48:55], v[84:87], v226, v225 op_sel_hi:[0,0,0]
	v_mfma_scale_f32_16x16x128_f8f6f4 v[80:83], v[24:31], v[48:55], v[80:83], v226, v225 op_sel_hi:[0,0,0]
	v_mfma_scale_f32_16x16x128_f8f6f4 v[68:71], v[16:23], v[56:63], v[68:71], v226, v225 op_sel_hi:[0,0,0]
	v_mfma_scale_f32_16x16x128_f8f6f4 v[64:67], v[24:31], v[56:63], v[64:67], v226, v225 op_sel_hi:[0,0,0]
	s_setprio 0
	s_barrier
	s_add_u32 s26, s26, 0x100
	s_addc_u32 s27, s27, 0
	s_cmp_gt_u32 s5, 5
	s_cbranch_scc1 .LBB0_502
	s_mov_b32 s5, s23
	s_branch .LBB0_497

.LBB0_986:
	s_cmpk_eq_i32 s10, 0x300
	s_cselect_b64 s[12:13], -1, 0
	s_add_i32 s14, 0, 0x10000
	v_add_u32_e64 v0, s14, v205
	s_add_i32 s15, 0, 0x14000
	v_add_u32_e64 v1, s14, v237
	ds_read_b128 v[8:11], v0
	ds_read_b128 v[12:15], v1
	v_add_u32_e32 v0, s76, v205
	v_add_u32_e32 v1, s76, v237
	ds_read_b128 v[24:27], v0
	ds_read_b128 v[28:31], v1
	v_add_u32_e32 v0, s15, v205
	v_add_u32_e32 v4, s15, v237
	v_add_u32_e32 v16, s77, v205
	v_add_u32_e32 v20, s77, v237
	ds_read_b128 v[0:3], v0
	ds_read_b128 v[4:7], v4
	ds_read_b128 v[16:19], v16
	ds_read_b128 v[20:23], v20
	s_add_i32 m0, s21, 0xc000
	s_add_u32 s14, s41, s10
	s_addc_u32 s15, s45, s11
	s_add_i32 s16, s21, 0xe000
	s_cmpk_lg_i32 s10, 0x300
	s_nop 0
	ds_read_b128 v[40:43], v239
	ds_read_b128 v[32:35], v239 offset:2048
	ds_read_b128 v[44:47], v240
	ds_read_b128 v[36:39], v240 offset:2048
	ds_read_b128 v[56:59], v239 offset:4096
	ds_read_b128 v[48:51], v239 offset:6144
	ds_read_b128 v[60:63], v240 offset:4096
	ds_read_b128 v[52:55], v240 offset:6144
	global_load_lds_dwordx4 v96, s[14:15]
	s_mov_b32 m0, s16
	s_nop 0
	global_load_lds_dwordx4 v206, s[14:15]
	s_waitcnt vmcnt(8)
	s_waitcnt lgkmcnt(0)
	s_barrier
	s_setprio 1
	s_waitcnt lgkmcnt(0)
	s_nop 0
	v_mfma_scale_f32_16x16x128_f8f6f4 v[186:189], v[8:15], v[40:47], v[186:189], v226, v225 op_sel_hi:[0,0,0]
	v_mfma_scale_f32_16x16x128_f8f6f4 v[190:193], v[24:31], v[40:47], v[190:193], v226, v225 op_sel_hi:[0,0,0]
	v_mfma_scale_f32_16x16x128_f8f6f4 v[174:177], v[8:15], v[32:39], v[174:177], v226, v225 op_sel_hi:[0,0,0]
	v_mfma_scale_f32_16x16x128_f8f6f4 v[170:173], v[24:31], v[32:39], v[170:173], v226, v225 op_sel_hi:[0,0,0]
	v_mfma_scale_f32_16x16x128_f8f6f4 v[158:161], v[8:15], v[56:63], v[158:161], v226, v225 op_sel_hi:[0,0,0]
	v_mfma_scale_f32_16x16x128_f8f6f4 v[154:157], v[24:31], v[56:63], v[154:157], v226, v225 op_sel_hi:[0,0,0]
	v_mfma_scale_f32_16x16x128_f8f6f4 v[142:145], v[8:15], v[48:55], v[142:145], v226, v225 op_sel_hi:[0,0,0]
	v_mfma_scale_f32_16x16x128_f8f6f4 v[138:141], v[24:31], v[48:55], v[138:141], v226, v225 op_sel_hi:[0,0,0]
	s_setprio 0
	s_setprio 1
	v_mfma_scale_f32_16x16x128_f8f6f4 v[182:185], v[0:7], v[40:47], v[182:185], v226, v225 op_sel_hi:[0,0,0]
	v_mfma_scale_f32_16x16x128_f8f6f4 v[178:181], v[16:23], v[40:47], v[178:181], v226, v225 op_sel_hi:[0,0,0]
	v_mfma_scale_f32_16x16x128_f8f6f4 v[166:169], v[0:7], v[32:39], v[166:169], v226, v225 op_sel_hi:[0,0,0]
	v_mfma_scale_f32_16x16x128_f8f6f4 v[162:165], v[16:23], v[32:39], v[162:165], v226, v225 op_sel_hi:[0,0,0]
	v_mfma_scale_f32_16x16x128_f8f6f4 v[150:153], v[0:7], v[56:63], v[150:153], v226, v225 op_sel_hi:[0,0,0]
	v_mfma_scale_f32_16x16x128_f8f6f4 v[146:149], v[16:23], v[56:63], v[146:149], v226, v225 op_sel_hi:[0,0,0]
	v_mfma_scale_f32_16x16x128_f8f6f4 v[134:137], v[0:7], v[48:55], v[134:137], v226, v225 op_sel_hi:[0,0,0]
	v_mfma_scale_f32_16x16x128_f8f6f4 v[130:133], v[16:23], v[48:55], v[130:133], v226, v225 op_sel_hi:[0,0,0]
	s_setprio 0
	s_barrier
	s_cbranch_scc1 .LBB0_988
	v_mov_b64_e32 v[212:213], v[210:211]
	v_mov_b64_e32 v[214:215], v[208:209]
	v_mov_b32_e32 v206, v210
	v_mov_b32_e32 v96, v208
	v_mov_b32_e32 v204, v243
	v_mov_b32_e32 v202, v224
	v_mov_b32_e32 v241, v210
	v_mov_b32_e32 v242, v208
	s_branch .LBB0_989

.LBB0_989:
	s_and_b64 s[14:15], s[8:9], s[12:13]
	s_add_i32 s52, s49, 2
	s_and_b64 s[12:13], s[12:13], exec
	s_cselect_b32 s96, 0, s52
	s_and_b64 s[12:13], s[14:15], exec
	s_cselect_b32 s12, s47, s23
	s_ashr_i32 s13, s12, 31
	s_lshl_b64 s[14:15], s[96:97], 7
	s_or_b32 s96, s96, 1
	s_lshl_b64 s[16:17], s[12:13], 18
	s_lshl_b64 s[12:13], s[96:97], 7
	s_add_u32 s53, s18, s16
	s_addc_u32 s54, s19, s17
	s_add_u32 s16, s53, s14
	s_addc_u32 s17, s54, s15
	v_lshl_add_u64 v[216:217], s[16:17], 0, v[194:195]
	s_mov_b32 m0, s24
	s_nop 0
	ds_read_b128 v[56:59], v239 offset:16384
	ds_read_b128 v[60:63], v240 offset:16384
	ds_read_b128 v[48:51], v239 offset:18432
	ds_read_b128 v[52:55], v240 offset:18432
	ds_read_b128 v[40:43], v239 offset:20480
	ds_read_b128 v[44:47], v240 offset:20480
	ds_read_b128 v[32:35], v239 offset:22528
	ds_read_b128 v[36:39], v240 offset:22528
	global_load_lds_dwordx4 v[216:217], off
	v_lshl_add_u64 v[216:217], s[16:17], 0, v[196:197]
	s_add_u32 s16, s16, 0x20000
	s_mov_b32 m0, s25
	s_addc_u32 s17, s17, 0
	global_load_lds_dwordx4 v[216:217], off
	v_lshl_add_u64 v[216:217], s[16:17], 0, v[194:195]
	s_mov_b32 m0, s26
	s_add_u32 s14, s78, s14
	global_load_lds_dwordx4 v[216:217], off
	v_lshl_add_u64 v[216:217], s[16:17], 0, v[196:197]
	s_mov_b32 m0, s27
	s_addc_u32 s15, s79, s15
	global_load_lds_dwordx4 v[216:217], off
	s_mov_b32 m0, s21
	s_nop 0
	global_load_lds_dwordx4 v202, s[14:15]
	s_mov_b32 m0, s28
	s_nop 0
	global_load_lds_dwordx4 v204, s[14:15]
	s_waitcnt vmcnt(8)
	s_waitcnt lgkmcnt(0)
	s_barrier
	s_setprio 1
	s_waitcnt lgkmcnt(0)
	s_nop 0
	v_mfma_scale_f32_16x16x128_f8f6f4 v[126:129], v[8:15], v[56:63], v[126:129], v226, v225 op_sel_hi:[0,0,0]
	v_mfma_scale_f32_16x16x128_f8f6f4 v[122:125], v[24:31], v[56:63], v[122:125], v226, v225 op_sel_hi:[0,0,0]
	v_mfma_scale_f32_16x16x128_f8f6f4 v[110:113], v[8:15], v[48:55], v[110:113], v226, v225 op_sel_hi:[0,0,0]
	v_mfma_scale_f32_16x16x128_f8f6f4 v[106:109], v[24:31], v[48:55], v[106:109], v226, v225 op_sel_hi:[0,0,0]
	v_mfma_scale_f32_16x16x128_f8f6f4 v[92:95], v[8:15], v[40:47], v[92:95], v226, v225 op_sel_hi:[0,0,0]
	v_mfma_scale_f32_16x16x128_f8f6f4 v[88:91], v[24:31], v[40:47], v[88:91], v226, v225 op_sel_hi:[0,0,0]
	v_mfma_scale_f32_16x16x128_f8f6f4 v[76:79], v[8:15], v[32:39], v[76:79], v226, v225 op_sel_hi:[0,0,0]
	v_mfma_scale_f32_16x16x128_f8f6f4 v[72:75], v[24:31], v[32:39], v[72:75], v226, v225 op_sel_hi:[0,0,0]
	s_setprio 0
	s_setprio 1
	v_mfma_scale_f32_16x16x128_f8f6f4 v[118:121], v[0:7], v[56:63], v[118:121], v226, v225 op_sel_hi:[0,0,0]
	v_mfma_scale_f32_16x16x128_f8f6f4 v[114:117], v[16:23], v[56:63], v[114:117], v226, v225 op_sel_hi:[0,0,0]
	v_mfma_scale_f32_16x16x128_f8f6f4 v[102:105], v[0:7], v[48:55], v[102:105], v226, v225 op_sel_hi:[0,0,0]
	v_mfma_scale_f32_16x16x128_f8f6f4 v[98:101], v[16:23], v[48:55], v[98:101], v226, v225 op_sel_hi:[0,0,0]
	v_mfma_scale_f32_16x16x128_f8f6f4 v[84:87], v[0:7], v[40:47], v[84:87], v226, v225 op_sel_hi:[0,0,0]
	v_mfma_scale_f32_16x16x128_f8f6f4 v[80:83], v[16:23], v[40:47], v[80:83], v226, v225 op_sel_hi:[0,0,0]
	v_mfma_scale_f32_16x16x128_f8f6f4 v[68:71], v[0:7], v[32:39], v[68:71], v226, v225 op_sel_hi:[0,0,0]
	v_mfma_scale_f32_16x16x128_f8f6f4 v[64:67], v[16:23], v[32:39], v[64:67], v226, v225 op_sel_hi:[0,0,0]
	s_setprio 0
	s_barrier
	s_add_i32 s16, 0, 0x18000
	s_add_i32 s17, 0, 0x1c000
	v_add_u32_e32 v0, s16, v205
	v_add_u32_e32 v4, s16, v237
	v_add_u32_e32 v8, s94, v205
	v_add_u32_e32 v12, s94, v237
	v_add_u32_e32 v16, s17, v205
	v_add_u32_e32 v20, s17, v237
	v_add_u32_e32 v24, s33, v205
	v_add_u32_e32 v28, s33, v237
	ds_read_b128 v[0:3], v0
	ds_read_b128 v[4:7], v4
	ds_read_b128 v[8:11], v8
	ds_read_b128 v[12:15], v12
	ds_read_b128 v[16:19], v16
	ds_read_b128 v[20:23], v20
	ds_read_b128 v[24:27], v24
	ds_read_b128 v[28:31], v28
	s_mov_b32 m0, s29
	s_nop 0
	v_lshl_add_u64 v[214:215], s[14:15], 0, v[214:215]
	ds_read_b128 v[32:35], v239 offset:32768
	ds_read_b128 v[40:43], v239 offset:34816
	ds_read_b128 v[36:39], v240 offset:32768
	ds_read_b128 v[44:47], v240 offset:34816
	ds_read_b128 v[48:51], v239 offset:36864
	ds_read_b128 v[56:59], v239 offset:38912
	ds_read_b128 v[52:55], v240 offset:36864
	ds_read_b128 v[60:63], v240 offset:38912
	global_load_lds_dwordx4 v[214:215], off
	v_lshl_add_u64 v[212:213], s[14:15], 0, v[212:213]
	s_mov_b32 m0, s30
	s_nop 0
	global_load_lds_dwordx4 v[212:213], off
	s_waitcnt vmcnt(8)
	s_waitcnt lgkmcnt(0)
	s_barrier
	s_setprio 1
	s_waitcnt lgkmcnt(0)
	s_nop 0
	v_mfma_scale_f32_16x16x128_f8f6f4 v[186:189], v[0:7], v[32:39], v[186:189], v226, v225 op_sel_hi:[0,0,0]
	v_mfma_scale_f32_16x16x128_f8f6f4 v[190:193], v[8:15], v[32:39], v[190:193], v226, v225 op_sel_hi:[0,0,0]
	v_mfma_scale_f32_16x16x128_f8f6f4 v[174:177], v[0:7], v[40:47], v[174:177], v226, v225 op_sel_hi:[0,0,0]
	v_mfma_scale_f32_16x16x128_f8f6f4 v[170:173], v[8:15], v[40:47], v[170:173], v226, v225 op_sel_hi:[0,0,0]
	v_mfma_scale_f32_16x16x128_f8f6f4 v[158:161], v[0:7], v[48:55], v[158:161], v226, v225 op_sel_hi:[0,0,0]
	v_mfma_scale_f32_16x16x128_f8f6f4 v[154:157], v[8:15], v[48:55], v[154:157], v226, v225 op_sel_hi:[0,0,0]
	v_mfma_scale_f32_16x16x128_f8f6f4 v[142:145], v[0:7], v[56:63], v[142:145], v226, v225 op_sel_hi:[0,0,0]
	v_mfma_scale_f32_16x16x128_f8f6f4 v[138:141], v[8:15], v[56:63], v[138:141], v226, v225 op_sel_hi:[0,0,0]
	s_setprio 0
	s_setprio 1
	v_mfma_scale_f32_16x16x128_f8f6f4 v[182:185], v[16:23], v[32:39], v[182:185], v226, v225 op_sel_hi:[0,0,0]
	v_mfma_scale_f32_16x16x128_f8f6f4 v[178:181], v[24:31], v[32:39], v[178:181], v226, v225 op_sel_hi:[0,0,0]
	v_mfma_scale_f32_16x16x128_f8f6f4 v[166:169], v[16:23], v[40:47], v[166:169], v226, v225 op_sel_hi:[0,0,0]
	v_mfma_scale_f32_16x16x128_f8f6f4 v[162:165], v[24:31], v[40:47], v[162:165], v226, v225 op_sel_hi:[0,0,0]
	v_mfma_scale_f32_16x16x128_f8f6f4 v[150:153], v[16:23], v[48:55], v[150:153], v226, v225 op_sel_hi:[0,0,0]
	v_mfma_scale_f32_16x16x128_f8f6f4 v[146:149], v[24:31], v[48:55], v[146:149], v226, v225 op_sel_hi:[0,0,0]
	v_mfma_scale_f32_16x16x128_f8f6f4 v[134:137], v[16:23], v[56:63], v[134:137], v226, v225 op_sel_hi:[0,0,0]
	v_mfma_scale_f32_16x16x128_f8f6f4 v[130:133], v[24:31], v[56:63], v[130:133], v226, v225 op_sel_hi:[0,0,0]
	s_setprio 0
	s_barrier
	s_add_u32 s14, s53, s12
	s_addc_u32 s15, s54, s13
	s_add_i32 s16, s16, s20
	s_nop 0
	v_lshl_add_u64 v[212:213], s[14:15], 0, v[194:195]
	s_mov_b32 m0, s16
	s_nop 0
	ds_read_b128 v[32:35], v239 offset:49152
	ds_read_b128 v[40:43], v239 offset:51200
	ds_read_b128 v[36:39], v240 offset:49152
	ds_read_b128 v[44:47], v240 offset:51200
	ds_read_b128 v[48:51], v239 offset:53248
	ds_read_b128 v[56:59], v239 offset:55296
	ds_read_b128 v[52:55], v240 offset:53248
	ds_read_b128 v[60:63], v240 offset:55296
	global_load_lds_dwordx4 v[212:213], off
	s_add_i32 m0, s16, 0x2000
	v_lshl_add_u64 v[212:213], s[14:15], 0, v[196:197]
	s_add_u32 s14, s14, 0x20000
	s_addc_u32 s15, s15, 0
	s_add_i32 s16, s17, s20
	global_load_lds_dwordx4 v[212:213], off
	v_lshl_add_u64 v[212:213], s[14:15], 0, v[194:195]
	s_mov_b32 m0, s16
	s_nop 0
	global_load_lds_dwordx4 v[212:213], off
	s_add_i32 m0, s16, 0x2000
	v_lshl_add_u64 v[212:213], s[14:15], 0, v[196:197]
	s_add_u32 s12, s78, s12
	s_nop 0
	global_load_lds_dwordx4 v[212:213], off
	s_addc_u32 s13, s79, s13
	s_mov_b32 m0, s39
	s_nop 0
	s_nop 0
	global_load_lds_dwordx4 v202, s[12:13]
	s_mov_b32 m0, s40
	s_nop 0
	global_load_lds_dwordx4 v204, s[12:13]
	s_waitcnt vmcnt(8)
	s_waitcnt lgkmcnt(0)
	s_barrier
	s_setprio 1
	s_waitcnt lgkmcnt(0)
	s_nop 0
	v_mfma_scale_f32_16x16x128_f8f6f4 v[126:129], v[0:7], v[32:39], v[126:129], v226, v225 op_sel_hi:[0,0,0]
	v_mfma_scale_f32_16x16x128_f8f6f4 v[122:125], v[8:15], v[32:39], v[122:125], v226, v225 op_sel_hi:[0,0,0]
	v_mfma_scale_f32_16x16x128_f8f6f4 v[110:113], v[0:7], v[40:47], v[110:113], v226, v225 op_sel_hi:[0,0,0]
	v_mfma_scale_f32_16x16x128_f8f6f4 v[106:109], v[8:15], v[40:47], v[106:109], v226, v225 op_sel_hi:[0,0,0]
	v_mfma_scale_f32_16x16x128_f8f6f4 v[92:95], v[0:7], v[48:55], v[92:95], v226, v225 op_sel_hi:[0,0,0]
	v_mfma_scale_f32_16x16x128_f8f6f4 v[88:91], v[8:15], v[48:55], v[88:91], v226, v225 op_sel_hi:[0,0,0]
	v_mfma_scale_f32_16x16x128_f8f6f4 v[76:79], v[0:7], v[56:63], v[76:79], v226, v225 op_sel_hi:[0,0,0]
	v_mfma_scale_f32_16x16x128_f8f6f4 v[72:75], v[8:15], v[56:63], v[72:75], v226, v225 op_sel_hi:[0,0,0]
	s_setprio 0
	s_setprio 1
	v_mfma_scale_f32_16x16x128_f8f6f4 v[118:121], v[16:23], v[32:39], v[118:121], v226, v225 op_sel_hi:[0,0,0]
	v_mfma_scale_f32_16x16x128_f8f6f4 v[114:117], v[24:31], v[32:39], v[114:117], v226, v225 op_sel_hi:[0,0,0]
	v_mfma_scale_f32_16x16x128_f8f6f4 v[102:105], v[16:23], v[40:47], v[102:105], v226, v225 op_sel_hi:[0,0,0]
	v_mfma_scale_f32_16x16x128_f8f6f4 v[98:101], v[24:31], v[40:47], v[98:101], v226, v225 op_sel_hi:[0,0,0]
	v_mfma_scale_f32_16x16x128_f8f6f4 v[84:87], v[16:23], v[48:55], v[84:87], v226, v225 op_sel_hi:[0,0,0]
	v_mfma_scale_f32_16x16x128_f8f6f4 v[80:83], v[24:31], v[48:55], v[80:83], v226, v225 op_sel_hi:[0,0,0]
	v_mfma_scale_f32_16x16x128_f8f6f4 v[68:71], v[16:23], v[56:63], v[68:71], v226, v225 op_sel_hi:[0,0,0]
	v_mfma_scale_f32_16x16x128_f8f6f4 v[64:67], v[24:31], v[56:63], v[64:67], v226, v225 op_sel_hi:[0,0,0]
	s_setprio 0
	s_barrier
	s_add_u32 s10, s10, 0x100
	s_addc_u32 s11, s11, 0
	s_cmp_gt_u32 s49, 5
	s_cbranch_scc1 .LBB0_991
	s_mov_b32 s49, s52
	s_branch .LBB0_986

.LBB0_1267:
	s_cmpk_eq_i32 s16, 0x300
	s_cselect_b64 s[18:19], -1, 0
	s_add_i32 s13, 0, 0x10000
	v_add_u32_e64 v0, s13, v209
	s_add_i32 s20, 0, 0x14000
	v_add_u32_e64 v1, s13, v239
	ds_read_b128 v[8:11], v0
	ds_read_b128 v[12:15], v1
	v_add_u32_e32 v0, s76, v209
	v_add_u32_e32 v1, s76, v239
	ds_read_b128 v[24:27], v0
	ds_read_b128 v[28:31], v1
	v_add_u32_e32 v0, s20, v209
	v_add_u32_e32 v4, s20, v239
	v_add_u32_e32 v16, s77, v209
	v_add_u32_e32 v20, s77, v239
	ds_read_b128 v[0:3], v0
	ds_read_b128 v[4:7], v4
	ds_read_b128 v[16:19], v16
	ds_read_b128 v[20:23], v20
	s_add_i32 m0, s40, 0xc000
	s_add_u32 s20, s65, s16
	s_addc_u32 s21, s80, s17
	s_add_i32 s13, s40, 0xe000
	s_cmpk_lg_i32 s16, 0x300
	s_nop 0
	ds_read_b128 v[40:43], v244
	ds_read_b128 v[32:35], v244 offset:2048
	ds_read_b128 v[44:47], v245
	ds_read_b128 v[36:39], v245 offset:2048
	ds_read_b128 v[56:59], v244 offset:4096
	ds_read_b128 v[48:51], v244 offset:6144
	ds_read_b128 v[60:63], v245 offset:4096
	ds_read_b128 v[52:55], v245 offset:6144
	global_load_lds_dwordx4 v96, s[20:21]
	s_mov_b32 m0, s13
	s_nop 0
	global_load_lds_dwordx4 v204, s[20:21]
	s_waitcnt vmcnt(8)
	s_waitcnt lgkmcnt(0)
	s_barrier
	s_setprio 1
	s_waitcnt lgkmcnt(0)
	s_nop 0
	v_mfma_scale_f32_16x16x128_f8f6f4 v[72:75], v[8:15], v[40:47], v[72:75], v226, v225 op_sel_hi:[0,0,0]
	v_mfma_scale_f32_16x16x128_f8f6f4 v[64:67], v[24:31], v[40:47], v[64:67], v226, v225 op_sel_hi:[0,0,0]
	v_mfma_scale_f32_16x16x128_f8f6f4 v[88:91], v[8:15], v[32:39], v[88:91], v226, v225 op_sel_hi:[0,0,0]
	v_mfma_scale_f32_16x16x128_f8f6f4 v[80:83], v[24:31], v[32:39], v[80:83], v226, v225 op_sel_hi:[0,0,0]
	v_mfma_scale_f32_16x16x128_f8f6f4 v[126:129], v[8:15], v[56:63], v[126:129], v226, v225 op_sel_hi:[0,0,0]
	v_mfma_scale_f32_16x16x128_f8f6f4 v[106:109], v[24:31], v[56:63], v[106:109], v226, v225 op_sel_hi:[0,0,0]
	v_mfma_scale_f32_16x16x128_f8f6f4 v[158:161], v[8:15], v[48:55], v[158:161], v226, v225 op_sel_hi:[0,0,0]
	v_mfma_scale_f32_16x16x128_f8f6f4 v[142:145], v[24:31], v[48:55], v[142:145], v226, v225 op_sel_hi:[0,0,0]
	s_setprio 0
	s_setprio 1
	v_mfma_scale_f32_16x16x128_f8f6f4 v[76:79], v[0:7], v[40:47], v[76:79], v226, v225 op_sel_hi:[0,0,0]
	v_mfma_scale_f32_16x16x128_f8f6f4 v[68:71], v[16:23], v[40:47], v[68:71], v226, v225 op_sel_hi:[0,0,0]
	v_mfma_scale_f32_16x16x128_f8f6f4 v[102:105], v[0:7], v[32:39], v[102:105], v226, v225 op_sel_hi:[0,0,0]
	v_mfma_scale_f32_16x16x128_f8f6f4 v[84:87], v[16:23], v[32:39], v[84:87], v226, v225 op_sel_hi:[0,0,0]
	v_mfma_scale_f32_16x16x128_f8f6f4 v[134:137], v[0:7], v[56:63], v[134:137], v226, v225 op_sel_hi:[0,0,0]
	v_mfma_scale_f32_16x16x128_f8f6f4 v[118:121], v[16:23], v[56:63], v[118:121], v226, v225 op_sel_hi:[0,0,0]
	v_mfma_scale_f32_16x16x128_f8f6f4 v[166:169], v[0:7], v[48:55], v[166:169], v226, v225 op_sel_hi:[0,0,0]
	v_mfma_scale_f32_16x16x128_f8f6f4 v[150:153], v[16:23], v[48:55], v[150:153], v226, v225 op_sel_hi:[0,0,0]
	s_setprio 0
	s_barrier
	s_cbranch_scc1 .LBB0_1269
	v_mov_b64_e32 v[214:215], v[212:213]
	v_mov_b64_e32 v[216:217], v[210:211]
	v_mov_b32_e32 v204, v212
	v_mov_b32_e32 v96, v210
	v_mov_b32_e32 v206, v224
	v_mov_b32_e32 v208, v250
	v_mov_b32_e32 v246, v212
	v_mov_b32_e32 v247, v210
	s_branch .LBB0_1270
.LBB0_1269:
	v_mov_b32_e64 v205, v97
	v_mov_b64_e32 v[214:215], v[204:205]
	v_mov_b64_e32 v[216:217], v[96:97]
.LBB0_1270:
	s_and_b64 s[20:21], s[14:15], s[18:19]
	s_add_i32 s13, s11, 2
	s_and_b64 s[18:19], s[18:19], exec
	s_cselect_b32 s96, 0, s13
	s_and_b64 s[18:19], s[20:21], exec
	s_cselect_b32 s18, s10, s12
	s_mul_hi_i32 s19, s18, 0x2aaaaaab
	s_cselect_b32 s20, s81, s93
	s_lshr_b32 s21, s19, 31
	s_add_i32 s19, s19, s21
	s_mul_i32 s21, s19, 6
	s_sub_i32 s18, s18, s21
	s_cmp_lt_u32 s18, 5
	s_cselect_b32 s21, 1, 2
	s_min_u32 s25, s18, 4
	s_add_i32 s24, s18, 1
	s_add_i32 s25, s25, -1
	s_cmp_lt_i32 s18, 3
	s_cselect_b32 s18, 0, s21
	s_cselect_b32 s21, s24, s25
	s_lshl_b32 s19, s19, 2
	s_or_b32 s18, s18, s19
	s_add_i32 s21, s21, s19
	s_cmp_lt_i32 s20, 4
	s_cselect_b32 s18, s18, s21
	s_lshl_b32 s20, s20, 18
	s_ashr_i32 s19, s18, 31
	s_and_b32 s53, s20, 0xc0000
	s_lshl_b64 s[20:21], s[96:97], 7
	s_or_b32 s96, s96, 1
	s_lshl_b64 s[24:25], s[18:19], 20
	s_lshl_b64 s[18:19], s[96:97], 7
	s_add_u32 s24, s31, s24
	s_addc_u32 s25, s38, s25
	s_add_u32 s53, s24, s53
	s_addc_u32 s72, s25, 0
	s_add_u32 s24, s53, s20
	s_addc_u32 s25, s72, s21
	v_lshl_add_u64 v[218:219], s[24:25], 0, v[196:197]
	s_mov_b32 m0, s41
	s_nop 0
	ds_read_b128 v[56:59], v244 offset:16384
	ds_read_b128 v[60:63], v245 offset:16384
	ds_read_b128 v[48:51], v244 offset:18432
	ds_read_b128 v[52:55], v245 offset:18432
	ds_read_b128 v[40:43], v244 offset:20480
	ds_read_b128 v[44:47], v245 offset:20480
	ds_read_b128 v[32:35], v244 offset:22528
	ds_read_b128 v[36:39], v245 offset:22528
	global_load_lds_dwordx4 v[218:219], off
	v_lshl_add_u64 v[218:219], s[24:25], 0, v[202:203]
	s_add_u32 s24, s24, 0x20000
	s_mov_b32 m0, s45
	s_addc_u32 s25, s25, 0
	global_load_lds_dwordx4 v[218:219], off
	v_lshl_add_u64 v[218:219], s[24:25], 0, v[196:197]
	s_mov_b32 m0, s48
	s_add_u32 s20, s78, s20
	global_load_lds_dwordx4 v[218:219], off
	v_lshl_add_u64 v[218:219], s[24:25], 0, v[202:203]
	s_mov_b32 m0, s49
	s_addc_u32 s21, s79, s21
	global_load_lds_dwordx4 v[218:219], off
	s_mov_b32 m0, s40
	s_nop 0
	global_load_lds_dwordx4 v208, s[20:21]
	s_mov_b32 m0, s57
	s_nop 0
	global_load_lds_dwordx4 v206, s[20:21]
	s_waitcnt vmcnt(8)
	s_waitcnt lgkmcnt(0)
	s_barrier
	s_setprio 1
	s_waitcnt lgkmcnt(0)
	s_nop 0
	v_mfma_scale_f32_16x16x128_f8f6f4 v[110:113], v[8:15], v[56:63], v[110:113], v226, v225 op_sel_hi:[0,0,0]
	v_mfma_scale_f32_16x16x128_f8f6f4 v[92:95], v[24:31], v[56:63], v[92:95], v226, v225 op_sel_hi:[0,0,0]
	v_mfma_scale_f32_16x16x128_f8f6f4 v[138:141], v[8:15], v[48:55], v[138:141], v226, v225 op_sel_hi:[0,0,0]
	v_mfma_scale_f32_16x16x128_f8f6f4 v[122:125], v[24:31], v[48:55], v[122:125], v226, v225 op_sel_hi:[0,0,0]
	v_mfma_scale_f32_16x16x128_f8f6f4 v[170:173], v[8:15], v[40:47], v[170:173], v226, v225 op_sel_hi:[0,0,0]
	v_mfma_scale_f32_16x16x128_f8f6f4 v[154:157], v[24:31], v[40:47], v[154:157], v226, v225 op_sel_hi:[0,0,0]
	v_mfma_scale_f32_16x16x128_f8f6f4 v[186:189], v[8:15], v[32:39], v[186:189], v226, v225 op_sel_hi:[0,0,0]
	v_mfma_scale_f32_16x16x128_f8f6f4 v[178:181], v[24:31], v[32:39], v[178:181], v226, v225 op_sel_hi:[0,0,0]
	s_setprio 0
	s_setprio 1
	v_mfma_scale_f32_16x16x128_f8f6f4 v[114:117], v[0:7], v[56:63], v[114:117], v226, v225 op_sel_hi:[0,0,0]
	v_mfma_scale_f32_16x16x128_f8f6f4 v[98:101], v[16:23], v[56:63], v[98:101], v226, v225 op_sel_hi:[0,0,0]
	v_mfma_scale_f32_16x16x128_f8f6f4 v[146:149], v[0:7], v[48:55], v[146:149], v226, v225 op_sel_hi:[0,0,0]
	v_mfma_scale_f32_16x16x128_f8f6f4 v[130:133], v[16:23], v[48:55], v[130:133], v226, v225 op_sel_hi:[0,0,0]
	v_mfma_scale_f32_16x16x128_f8f6f4 v[174:177], v[0:7], v[40:47], v[174:177], v226, v225 op_sel_hi:[0,0,0]
	v_mfma_scale_f32_16x16x128_f8f6f4 v[162:165], v[16:23], v[40:47], v[162:165], v226, v225 op_sel_hi:[0,0,0]
	v_mfma_scale_f32_16x16x128_f8f6f4 v[190:193], v[0:7], v[32:39], v[190:193], v226, v225 op_sel_hi:[0,0,0]
	v_mfma_scale_f32_16x16x128_f8f6f4 v[182:185], v[16:23], v[32:39], v[182:185], v226, v225 op_sel_hi:[0,0,0]
	s_setprio 0
	s_barrier
	s_add_i32 s24, 0, 0x18000
	s_add_i32 s25, 0, 0x1c000
	v_add_u32_e32 v0, s24, v209
	v_add_u32_e32 v4, s24, v239
	v_add_u32_e32 v8, s94, v209
	v_add_u32_e32 v12, s94, v239
	v_add_u32_e32 v16, s25, v209
	v_add_u32_e32 v20, s25, v239
	v_add_u32_e32 v24, s33, v209
	v_add_u32_e32 v28, s33, v239
	ds_read_b128 v[0:3], v0
	ds_read_b128 v[4:7], v4
	ds_read_b128 v[8:11], v8
	ds_read_b128 v[12:15], v12
	ds_read_b128 v[16:19], v16
	ds_read_b128 v[20:23], v20
	ds_read_b128 v[24:27], v24
	ds_read_b128 v[28:31], v28
	s_mov_b32 m0, s58
	s_nop 0
	v_lshl_add_u64 v[216:217], s[20:21], 0, v[216:217]
	ds_read_b128 v[32:35], v244 offset:32768
	ds_read_b128 v[40:43], v244 offset:34816
	ds_read_b128 v[36:39], v245 offset:32768
	ds_read_b128 v[44:47], v245 offset:34816
	ds_read_b128 v[48:51], v244 offset:36864
	ds_read_b128 v[56:59], v244 offset:38912
	ds_read_b128 v[52:55], v245 offset:36864
	ds_read_b128 v[60:63], v245 offset:38912
	global_load_lds_dwordx4 v[216:217], off
	v_lshl_add_u64 v[214:215], s[20:21], 0, v[214:215]
	s_mov_b32 m0, s59
	s_nop 0
	global_load_lds_dwordx4 v[214:215], off
	s_waitcnt vmcnt(8)
	s_waitcnt lgkmcnt(0)
	s_barrier
	s_setprio 1
	s_waitcnt lgkmcnt(0)
	s_nop 0
	v_mfma_scale_f32_16x16x128_f8f6f4 v[72:75], v[0:7], v[32:39], v[72:75], v226, v225 op_sel_hi:[0,0,0]
	v_mfma_scale_f32_16x16x128_f8f6f4 v[64:67], v[8:15], v[32:39], v[64:67], v226, v225 op_sel_hi:[0,0,0]
	v_mfma_scale_f32_16x16x128_f8f6f4 v[88:91], v[0:7], v[40:47], v[88:91], v226, v225 op_sel_hi:[0,0,0]
	v_mfma_scale_f32_16x16x128_f8f6f4 v[80:83], v[8:15], v[40:47], v[80:83], v226, v225 op_sel_hi:[0,0,0]
	v_mfma_scale_f32_16x16x128_f8f6f4 v[126:129], v[0:7], v[48:55], v[126:129], v226, v225 op_sel_hi:[0,0,0]
	v_mfma_scale_f32_16x16x128_f8f6f4 v[106:109], v[8:15], v[48:55], v[106:109], v226, v225 op_sel_hi:[0,0,0]
	v_mfma_scale_f32_16x16x128_f8f6f4 v[158:161], v[0:7], v[56:63], v[158:161], v226, v225 op_sel_hi:[0,0,0]
	v_mfma_scale_f32_16x16x128_f8f6f4 v[142:145], v[8:15], v[56:63], v[142:145], v226, v225 op_sel_hi:[0,0,0]
	s_setprio 0
	s_setprio 1
	v_mfma_scale_f32_16x16x128_f8f6f4 v[76:79], v[16:23], v[32:39], v[76:79], v226, v225 op_sel_hi:[0,0,0]
	v_mfma_scale_f32_16x16x128_f8f6f4 v[68:71], v[24:31], v[32:39], v[68:71], v226, v225 op_sel_hi:[0,0,0]
	v_mfma_scale_f32_16x16x128_f8f6f4 v[102:105], v[16:23], v[40:47], v[102:105], v226, v225 op_sel_hi:[0,0,0]
	v_mfma_scale_f32_16x16x128_f8f6f4 v[84:87], v[24:31], v[40:47], v[84:87], v226, v225 op_sel_hi:[0,0,0]
	v_mfma_scale_f32_16x16x128_f8f6f4 v[134:137], v[16:23], v[48:55], v[134:137], v226, v225 op_sel_hi:[0,0,0]
	v_mfma_scale_f32_16x16x128_f8f6f4 v[118:121], v[24:31], v[48:55], v[118:121], v226, v225 op_sel_hi:[0,0,0]
	v_mfma_scale_f32_16x16x128_f8f6f4 v[166:169], v[16:23], v[56:63], v[166:169], v226, v225 op_sel_hi:[0,0,0]
	v_mfma_scale_f32_16x16x128_f8f6f4 v[150:153], v[24:31], v[56:63], v[150:153], v226, v225 op_sel_hi:[0,0,0]
	s_setprio 0
	s_barrier
	s_add_u32 s20, s53, s18
	s_addc_u32 s21, s72, s19
	s_add_i32 s24, s24, s39
	s_nop 0
	v_lshl_add_u64 v[214:215], s[20:21], 0, v[196:197]
	s_mov_b32 m0, s24
	s_nop 0
	ds_read_b128 v[32:35], v244 offset:49152
	ds_read_b128 v[40:43], v244 offset:51200
	ds_read_b128 v[36:39], v245 offset:49152
	ds_read_b128 v[44:47], v245 offset:51200
	ds_read_b128 v[48:51], v244 offset:53248
	ds_read_b128 v[56:59], v244 offset:55296
	ds_read_b128 v[52:55], v245 offset:53248
	ds_read_b128 v[60:63], v245 offset:55296
	global_load_lds_dwordx4 v[214:215], off
	s_add_i32 m0, s24, 0x2000
	v_lshl_add_u64 v[214:215], s[20:21], 0, v[202:203]
	s_add_u32 s20, s20, 0x20000
	s_addc_u32 s21, s21, 0
	s_add_i32 s24, s25, s39
	global_load_lds_dwordx4 v[214:215], off
	v_lshl_add_u64 v[214:215], s[20:21], 0, v[196:197]
	s_mov_b32 m0, s24
	s_nop 0
	global_load_lds_dwordx4 v[214:215], off
	s_add_i32 m0, s24, 0x2000
	v_lshl_add_u64 v[214:215], s[20:21], 0, v[202:203]
	s_add_u32 s18, s78, s18
	s_nop 0
	global_load_lds_dwordx4 v[214:215], off
	s_addc_u32 s19, s79, s19
	s_mov_b32 m0, s60
	s_nop 0
	s_nop 0
	global_load_lds_dwordx4 v208, s[18:19]
	s_mov_b32 m0, s61
	s_nop 0
	global_load_lds_dwordx4 v206, s[18:19]
	s_waitcnt vmcnt(8)
	s_waitcnt lgkmcnt(0)
	s_barrier
	s_setprio 1
	s_waitcnt lgkmcnt(0)
	s_nop 0
	v_mfma_scale_f32_16x16x128_f8f6f4 v[110:113], v[0:7], v[32:39], v[110:113], v226, v225 op_sel_hi:[0,0,0]
	v_mfma_scale_f32_16x16x128_f8f6f4 v[92:95], v[8:15], v[32:39], v[92:95], v226, v225 op_sel_hi:[0,0,0]
	v_mfma_scale_f32_16x16x128_f8f6f4 v[138:141], v[0:7], v[40:47], v[138:141], v226, v225 op_sel_hi:[0,0,0]
	v_mfma_scale_f32_16x16x128_f8f6f4 v[122:125], v[8:15], v[40:47], v[122:125], v226, v225 op_sel_hi:[0,0,0]
	v_mfma_scale_f32_16x16x128_f8f6f4 v[170:173], v[0:7], v[48:55], v[170:173], v226, v225 op_sel_hi:[0,0,0]
	v_mfma_scale_f32_16x16x128_f8f6f4 v[154:157], v[8:15], v[48:55], v[154:157], v226, v225 op_sel_hi:[0,0,0]
	v_mfma_scale_f32_16x16x128_f8f6f4 v[186:189], v[0:7], v[56:63], v[186:189], v226, v225 op_sel_hi:[0,0,0]
	v_mfma_scale_f32_16x16x128_f8f6f4 v[178:181], v[8:15], v[56:63], v[178:181], v226, v225 op_sel_hi:[0,0,0]
	s_setprio 0
	s_setprio 1
	v_mfma_scale_f32_16x16x128_f8f6f4 v[114:117], v[16:23], v[32:39], v[114:117], v226, v225 op_sel_hi:[0,0,0]
	v_mfma_scale_f32_16x16x128_f8f6f4 v[98:101], v[24:31], v[32:39], v[98:101], v226, v225 op_sel_hi:[0,0,0]
	v_mfma_scale_f32_16x16x128_f8f6f4 v[146:149], v[16:23], v[40:47], v[146:149], v226, v225 op_sel_hi:[0,0,0]
	v_mfma_scale_f32_16x16x128_f8f6f4 v[130:133], v[24:31], v[40:47], v[130:133], v226, v225 op_sel_hi:[0,0,0]
	v_mfma_scale_f32_16x16x128_f8f6f4 v[174:177], v[16:23], v[48:55], v[174:177], v226, v225 op_sel_hi:[0,0,0]
	v_mfma_scale_f32_16x16x128_f8f6f4 v[162:165], v[24:31], v[48:55], v[162:165], v226, v225 op_sel_hi:[0,0,0]
	v_mfma_scale_f32_16x16x128_f8f6f4 v[190:193], v[16:23], v[56:63], v[190:193], v226, v225 op_sel_hi:[0,0,0]
	v_mfma_scale_f32_16x16x128_f8f6f4 v[182:185], v[24:31], v[56:63], v[182:185], v226, v225 op_sel_hi:[0,0,0]
	s_setprio 0
	s_barrier
	s_add_u32 s16, s16, 0x100
	s_addc_u32 s17, s17, 0
	s_cmp_gt_u32 s11, 5
	s_cbranch_scc1 .LBB0_1272
	s_mov_b32 s11, s13
	s_branch .LBB0_1267

.LBB0_1474:
	s_lshl_b32 s26, s21, 6
	s_ashr_i32 s27, s26, 31
	s_lshl_b64 s[26:27], s[26:27], 2
	s_add_u32 s26, s4, s26
	v_mov_b32_e32 v211, v97
	v_mov_b32_e32 v209, v97
	s_addc_u32 s27, s5, s27
	s_mov_b32 s13, 0
	s_nop 0
.LBB0_1475:
	s_cmp_eq_u32 s13, 6
	s_cselect_b64 s[30:31], -1, 0
	s_and_b64 s[28:29], s[24:25], s[30:31]
	s_andn2_b64 vcc, exec, s[28:29]
	s_cbranch_vccnz .LBB0_1502
	s_and_b64 vcc, exec, s[0:1]
	s_cbranch_vccnz .LBB0_1501
	v_mov_b32_e32 v0, s51
	ds_read_b32 v0, v0
	s_waitcnt lgkmcnt(0)
	v_cmp_ne_u32_e32 vcc, 0, v0
	s_cbranch_vccnz .LBB0_1501
	s_nop 0
	s_memrealtime s[38:39]
	s_mov_b32 s15, 1
	s_branch .LBB0_1481

.LBB0_1481:
	s_nop 0
	global_load_dword v0, v97, s[26:27] sc1
	s_mov_b64 s[40:41], -1
	s_waitcnt vmcnt(0)
	v_readfirstlane_b32 s48, v0
	s_cmp_ge_u32 s48, s69
	s_mov_b64 s[48:49], -1
	s_cbranch_scc1 .LBB0_1480
	s_and_b32 s40, s15, 0xff
	s_cmp_lg_u32 s40, 0
	s_cselect_b64 s[48:49], -1, 0
	s_cmp_eq_u32 s40, 0
	s_cbranch_scc1 .LBB0_1484
	s_mov_b64 s[40:41], -1
	s_andn2_b64 vcc, exec, s[48:49]
	s_mov_b64 s[48:49], -1
	s_cbranch_vccnz .LBB0_1480
	s_branch .LBB0_1485
.LBB0_1484:
	s_nop 0
	global_load_dword v0, v97, s[8:9] sc1
	s_waitcnt vmcnt(0)
	v_readfirstlane_b32 s40, v0
	s_cmp_eq_u32 s40, 0
	s_cselect_b64 s[48:49], -1, 0
	s_mov_b64 s[40:41], -1
	s_andn2_b64 vcc, exec, s[48:49]
	s_mov_b64 s[48:49], -1
	s_cbranch_vccnz .LBB0_1480

.LBB0_1489:
	v_cmp_gt_i32_e32 vcc, s58, v227
	s_waitcnt lgkmcnt(0)
	s_mov_b64 s[38:39], -1
	s_mov_b64 s[40:41], -1
	s_and_saveexec_b64 s[48:49], vcc
	s_cbranch_execz .LBB0_1491
	v_lshlrev_b32_e32 v0, 8, v227
	s_nop 0
	global_load_dword v0, v0, s[4:5] sc1
	s_waitcnt vmcnt(0)
	v_cmp_le_u32_e32 vcc, s69, v0
	s_orn2_b64 s[40:41], vcc, exec
.LBB0_1491:
	s_or_b64 exec, exec, s[48:49]
	v_add_u32_e64 v0, 64, v227
	v_cmp_gt_i32_e32 vcc, s58, v0
	s_and_saveexec_b64 s[48:49], vcc
	s_cbranch_execz .LBB0_1493
	v_lshlrev_b32_e32 v0, 8, v0
	global_load_dword v0, v0, s[4:5] sc1
	s_waitcnt vmcnt(0)
	v_cmp_le_u32_e32 vcc, s69, v0
	s_orn2_b64 s[38:39], vcc, exec

.LBB0_1497:
	s_or_b64 exec, exec, s[54:55]
	v_or_b32_e32 v0, 0x100, v227
	v_cmp_gt_i32_e32 vcc, s58, v0
	s_mov_b64 s[54:55], -1
	s_and_saveexec_b64 s[56:57], vcc
	s_cbranch_execz .LBB0_1499
	v_lshlrev_b32_e32 v0, 8, v0
	s_nop 0
	global_load_dword v0, v0, s[4:5] sc1
	s_waitcnt vmcnt(0)
	v_cmp_le_u32_e32 vcc, s69, v0
	s_orn2_b64 s[54:55], vcc, exec
.LBB0_1499:
	s_or_b64 exec, exec, s[56:57]
	s_and_b64 s[38:39], s[40:41], s[38:39]
	s_and_b64 s[38:39], s[38:39], s[52:53]
	s_and_b64 s[38:39], s[38:39], s[48:49]
	s_and_b64 s[38:39], s[38:39], s[54:55]
	s_xor_b64 s[38:39], s[38:39], -1
	s_waitcnt vmcnt(0)
	buffer_inv sc1
	s_waitcnt vmcnt(0)
	s_nop 0
	v_cndmask_b32_e64 v0, 0, 1, s[38:39]
	v_cmp_ne_u32_e32 vcc, 0, v0
	s_cbranch_vccnz .LBB0_1501
	v_mov_b32_e32 v0, s51
	v_mov_b32_e32 v1, 1
	ds_write_b32 v0, v1

.LBB0_1502:
	s_nop 0
	s_add_i32 s15, 0, 0x10000
	v_add_u32_e32 v0, s15, v197
	v_add_u32_e32 v4, s15, v237
	v_add_u32_e64 v8, s76, v197
	s_add_i32 s15, 0, 0x14000
	ds_read_b128 v[0:3], v0
	ds_read_b128 v[4:7], v4
	v_add_u32_e64 v9, s76, v237
	ds_read_b128 v[16:19], v8
	ds_read_b128 v[20:23], v9
	v_add_u32_e32 v8, s15, v197
	v_add_u32_e32 v12, s15, v237
	v_add_u32_e32 v24, s77, v197
	v_add_u32_e32 v28, s77, v237
	ds_read_b128 v[8:11], v8
	ds_read_b128 v[12:15], v12
	ds_read_b128 v[24:27], v24
	ds_read_b128 v[28:31], v28
	s_or_b32 s96, s13, 1
	s_lshl_b64 s[38:39], s[96:97], 7
	s_add_u32 s38, s34, s38
	s_addc_u32 s39, s35, s39
	s_add_i32 m0, s11, 0xc000
	ds_read_b128 v[40:43], v248
	ds_read_b128 v[32:35], v248 offset:2048
	ds_read_b128 v[44:47], v249
	ds_read_b128 v[36:39], v249 offset:2048
	ds_read_b128 v[56:59], v248 offset:4096
	ds_read_b128 v[48:51], v248 offset:6144
	ds_read_b128 v[60:63], v249 offset:4096
	ds_read_b128 v[52:55], v249 offset:6144
	global_load_lds_dwordx4 v96, s[38:39]
	s_add_i32 m0, s11, 0xe000
	s_nop 0
	s_nop 0
	global_load_lds_dwordx4 v202, s[38:39]
	s_waitcnt vmcnt(8)
	s_waitcnt lgkmcnt(0)
	s_barrier
	s_setprio 1
	s_waitcnt lgkmcnt(0)
	s_nop 0
	v_mfma_scale_f32_16x16x128_f8f6f4 v[190:193], v[0:7], v[40:47], v[190:193], v226, v228 op_sel_hi:[0,0,0]
	v_mfma_scale_f32_16x16x128_f8f6f4 v[186:189], v[16:23], v[40:47], v[186:189], v226, v228 op_sel_hi:[0,0,0]
	v_mfma_scale_f32_16x16x128_f8f6f4 v[182:185], v[0:7], v[32:39], v[182:185], v226, v228 op_sel_hi:[0,0,0]
	v_mfma_scale_f32_16x16x128_f8f6f4 v[178:181], v[16:23], v[32:39], v[178:181], v226, v228 op_sel_hi:[0,0,0]
	v_mfma_scale_f32_16x16x128_f8f6f4 v[174:177], v[0:7], v[56:63], v[174:177], v226, v228 op_sel_hi:[0,0,0]
	v_mfma_scale_f32_16x16x128_f8f6f4 v[170:173], v[16:23], v[56:63], v[170:173], v226, v228 op_sel_hi:[0,0,0]
	v_mfma_scale_f32_16x16x128_f8f6f4 v[166:169], v[0:7], v[48:55], v[166:169], v226, v228 op_sel_hi:[0,0,0]
	v_mfma_scale_f32_16x16x128_f8f6f4 v[154:157], v[16:23], v[48:55], v[154:157], v226, v228 op_sel_hi:[0,0,0]
	s_setprio 0
	s_setprio 1
	v_mfma_scale_f32_16x16x128_f8f6f4 v[162:165], v[8:15], v[40:47], v[162:165], v226, v228 op_sel_hi:[0,0,0]
	v_mfma_scale_f32_16x16x128_f8f6f4 v[158:161], v[24:31], v[40:47], v[158:161], v226, v228 op_sel_hi:[0,0,0]
	v_mfma_scale_f32_16x16x128_f8f6f4 v[150:153], v[8:15], v[32:39], v[150:153], v226, v228 op_sel_hi:[0,0,0]
	v_mfma_scale_f32_16x16x128_f8f6f4 v[146:149], v[24:31], v[32:39], v[146:149], v226, v228 op_sel_hi:[0,0,0]
	v_mfma_scale_f32_16x16x128_f8f6f4 v[142:145], v[8:15], v[56:63], v[142:145], v226, v228 op_sel_hi:[0,0,0]
	v_mfma_scale_f32_16x16x128_f8f6f4 v[138:141], v[24:31], v[56:63], v[138:141], v226, v228 op_sel_hi:[0,0,0]
	v_mfma_scale_f32_16x16x128_f8f6f4 v[134:137], v[8:15], v[48:55], v[134:137], v226, v228 op_sel_hi:[0,0,0]
	v_mfma_scale_f32_16x16x128_f8f6f4 v[130:133], v[24:31], v[48:55], v[130:133], v226, v228 op_sel_hi:[0,0,0]
	s_setprio 0
	s_barrier
	s_andn2_b64 vcc, exec, s[30:31]
	s_cbranch_vccnz .LBB0_1504
	v_mov_b64_e32 v[212:213], v[208:209]
	v_mov_b64_e32 v[214:215], v[210:211]
	v_mov_b32_e32 v202, v208
	v_mov_b32_e32 v96, v210
	v_mov_b32_e32 v196, v224
	v_mov_b32_e32 v194, v236
	v_mov_b32_e64 v250, v208
	v_mov_b32_e32 v251, v210
	s_branch .LBB0_1505

.LBB0_1505:
	s_add_i32 s15, s13, 2
	s_and_b64 s[30:31], s[30:31], exec
	s_cselect_b32 s96, 0, s15
	s_and_b64 s[30:31], s[28:29], exec
	s_cselect_b32 s30, s80, s14
	s_mul_hi_i32 s31, s30, 0x2aaaaaab
	s_lshr_b32 s38, s31, 31
	s_add_i32 s31, s31, s38
	s_mul_i32 s38, s31, 6
	s_sub_i32 s30, s30, s38
	s_cmp_lt_u32 s30, 5
	s_cselect_b32 s38, 1, 2
	s_min_u32 s40, s30, 4
	s_add_i32 s39, s30, 1
	s_add_i32 s40, s40, -1
	s_cmp_lt_i32 s30, 3
	s_cselect_b32 s30, 0, s38
	s_cselect_b32 s38, s39, s40
	s_lshl_b32 s31, s31, 2
	s_or_b32 s30, s30, s31
	s_add_i32 s38, s38, s31
	s_cmp_lt_u32 s96, 4
	s_cselect_b32 s30, s30, s38
	s_ashr_i32 s31, s30, 31
	s_and_b64 s[28:29], s[28:29], exec
	s_cselect_b32 s28, s20, s10
	s_ashr_i32 s29, s28, 31
	s_lshl_b64 s[38:39], s[28:29], 17
	s_lshl_b32 s28, s96, 7
	s_nop 0
	s_and_b32 s40, s28, 0x100
	s_or_b32 s28, s96, 1
	s_lshl_b32 s29, s28, 7
	s_lshl_b64 s[30:31], s[30:31], 19
	s_nop 0
	s_and_b32 s29, s29, 0x180
	s_add_u32 s30, s59, s30
	s_addc_u32 s31, s60, s31
	s_add_u32 s38, s30, s38
	s_addc_u32 s39, s31, s39
	s_add_u32 s30, s38, s40
	s_addc_u32 s31, s39, 0
	v_lshl_add_u64 v[216:217], s[30:31], 0, v[204:205]
	s_mov_b32 m0, s92
	s_nop 0
	ds_read_b128 v[56:59], v248 offset:16384
	ds_read_b128 v[60:63], v249 offset:16384
	ds_read_b128 v[48:51], v248 offset:18432
	ds_read_b128 v[52:55], v249 offset:18432
	ds_read_b128 v[40:43], v248 offset:20480
	ds_read_b128 v[44:47], v249 offset:20480
	ds_read_b128 v[32:35], v248 offset:22528
	ds_read_b128 v[36:39], v249 offset:22528
	global_load_lds_dwordx4 v[216:217], off
	v_lshl_add_u64 v[216:217], s[30:31], 0, v[206:207]
	s_add_u32 s30, s30, 0x10000
	s_mov_b32 m0, s61
	s_addc_u32 s31, s31, 0
	global_load_lds_dwordx4 v[216:217], off
	v_lshl_add_u64 v[216:217], s[30:31], 0, v[204:205]
	s_mov_b32 m0, s64
	s_nop 0
	global_load_lds_dwordx4 v[216:217], off
	v_lshl_add_u64 v[216:217], s[30:31], 0, v[206:207]
	s_lshl_b64 s[30:31], s[96:97], 7
	s_mov_b32 m0, s45
	s_add_u32 s30, s34, s30
	s_nop 0
	global_load_lds_dwordx4 v[216:217], off
	s_addc_u32 s31, s35, s31
	s_mov_b32 m0, s11
	s_nop 0
	s_nop 0
	global_load_lds_dwordx4 v194, s[30:31]
	s_mov_b32 m0, s79
	s_nop 0
	global_load_lds_dwordx4 v196, s[30:31]
	s_waitcnt vmcnt(8)
	s_waitcnt lgkmcnt(0)
	s_barrier
	s_setprio 1
	s_waitcnt lgkmcnt(0)
	s_nop 0
	v_mfma_scale_f32_16x16x128_f8f6f4 v[126:129], v[0:7], v[56:63], v[126:129], v226, v228 op_sel_hi:[0,0,0]
	v_mfma_scale_f32_16x16x128_f8f6f4 v[122:125], v[16:23], v[56:63], v[122:125], v226, v228 op_sel_hi:[0,0,0]
	v_mfma_scale_f32_16x16x128_f8f6f4 v[118:121], v[0:7], v[48:55], v[118:121], v226, v228 op_sel_hi:[0,0,0]
	v_mfma_scale_f32_16x16x128_f8f6f4 v[114:117], v[16:23], v[48:55], v[114:117], v226, v228 op_sel_hi:[0,0,0]
	v_mfma_scale_f32_16x16x128_f8f6f4 v[110:113], v[0:7], v[40:47], v[110:113], v226, v228 op_sel_hi:[0,0,0]
	v_mfma_scale_f32_16x16x128_f8f6f4 v[106:109], v[16:23], v[40:47], v[106:109], v226, v228 op_sel_hi:[0,0,0]
	v_mfma_scale_f32_16x16x128_f8f6f4 v[102:105], v[0:7], v[32:39], v[102:105], v226, v228 op_sel_hi:[0,0,0]
	v_mfma_scale_f32_16x16x128_f8f6f4 v[98:101], v[16:23], v[32:39], v[98:101], v226, v228 op_sel_hi:[0,0,0]
	s_setprio 0
	s_setprio 1
	v_mfma_scale_f32_16x16x128_f8f6f4 v[92:95], v[8:15], v[56:63], v[92:95], v226, v228 op_sel_hi:[0,0,0]
	v_mfma_scale_f32_16x16x128_f8f6f4 v[88:91], v[24:31], v[56:63], v[88:91], v226, v228 op_sel_hi:[0,0,0]
	v_mfma_scale_f32_16x16x128_f8f6f4 v[84:87], v[8:15], v[48:55], v[84:87], v226, v228 op_sel_hi:[0,0,0]
	v_mfma_scale_f32_16x16x128_f8f6f4 v[80:83], v[24:31], v[48:55], v[80:83], v226, v228 op_sel_hi:[0,0,0]
	v_mfma_scale_f32_16x16x128_f8f6f4 v[76:79], v[8:15], v[40:47], v[76:79], v226, v228 op_sel_hi:[0,0,0]
	v_mfma_scale_f32_16x16x128_f8f6f4 v[72:75], v[24:31], v[40:47], v[72:75], v226, v228 op_sel_hi:[0,0,0]
	v_mfma_scale_f32_16x16x128_f8f6f4 v[68:71], v[8:15], v[32:39], v[68:71], v226, v228 op_sel_hi:[0,0,0]
	v_mfma_scale_f32_16x16x128_f8f6f4 v[64:67], v[24:31], v[32:39], v[64:67], v226, v228 op_sel_hi:[0,0,0]
	s_setprio 0
	s_barrier
	s_add_i32 s40, 0, 0x18000
	s_add_i32 s41, 0, 0x1c000
	v_add_u32_e32 v0, s40, v197
	v_add_u32_e32 v4, s40, v237
	v_add_u32_e32 v8, s94, v197
	v_add_u32_e32 v12, s94, v237
	v_add_u32_e32 v16, s41, v197
	v_add_u32_e32 v20, s41, v237
	v_add_u32_e32 v24, s33, v197
	v_add_u32_e32 v28, s33, v237
	ds_read_b128 v[0:3], v0
	ds_read_b128 v[4:7], v4
	ds_read_b128 v[8:11], v8
	ds_read_b128 v[12:15], v12
	ds_read_b128 v[16:19], v16
	ds_read_b128 v[20:23], v20
	ds_read_b128 v[24:27], v24
	ds_read_b128 v[28:31], v28
	s_mov_b32 m0, s93
	s_nop 0
	v_lshl_add_u64 v[214:215], s[30:31], 0, v[214:215]
	ds_read_b128 v[32:35], v248 offset:32768
	ds_read_b128 v[40:43], v248 offset:34816
	ds_read_b128 v[36:39], v249 offset:32768
	ds_read_b128 v[44:47], v249 offset:34816
	ds_read_b128 v[48:51], v248 offset:36864
	ds_read_b128 v[56:59], v248 offset:38912
	ds_read_b128 v[52:55], v249 offset:36864
	ds_read_b128 v[60:63], v249 offset:38912
	global_load_lds_dwordx4 v[214:215], off
	v_lshl_add_u64 v[212:213], s[30:31], 0, v[212:213]
	s_mov_b32 m0, s65
	s_nop 0
	global_load_lds_dwordx4 v[212:213], off
	s_waitcnt vmcnt(8)
	s_waitcnt lgkmcnt(0)
	s_barrier
	s_setprio 1
	s_waitcnt lgkmcnt(0)
	s_nop 0
	v_mfma_scale_f32_16x16x128_f8f6f4 v[190:193], v[0:7], v[32:39], v[190:193], v226, v228 op_sel_hi:[0,0,0]
	v_mfma_scale_f32_16x16x128_f8f6f4 v[186:189], v[8:15], v[32:39], v[186:189], v226, v228 op_sel_hi:[0,0,0]
	v_mfma_scale_f32_16x16x128_f8f6f4 v[182:185], v[0:7], v[40:47], v[182:185], v226, v228 op_sel_hi:[0,0,0]
	v_mfma_scale_f32_16x16x128_f8f6f4 v[178:181], v[8:15], v[40:47], v[178:181], v226, v228 op_sel_hi:[0,0,0]
	v_mfma_scale_f32_16x16x128_f8f6f4 v[174:177], v[0:7], v[48:55], v[174:177], v226, v228 op_sel_hi:[0,0,0]
	v_mfma_scale_f32_16x16x128_f8f6f4 v[170:173], v[8:15], v[48:55], v[170:173], v226, v228 op_sel_hi:[0,0,0]
	v_mfma_scale_f32_16x16x128_f8f6f4 v[166:169], v[0:7], v[56:63], v[166:169], v226, v228 op_sel_hi:[0,0,0]
	v_mfma_scale_f32_16x16x128_f8f6f4 v[154:157], v[8:15], v[56:63], v[154:157], v226, v228 op_sel_hi:[0,0,0]
	s_setprio 0
	s_setprio 1
	v_mfma_scale_f32_16x16x128_f8f6f4 v[162:165], v[16:23], v[32:39], v[162:165], v226, v228 op_sel_hi:[0,0,0]
	v_mfma_scale_f32_16x16x128_f8f6f4 v[158:161], v[24:31], v[32:39], v[158:161], v226, v228 op_sel_hi:[0,0,0]
	v_mfma_scale_f32_16x16x128_f8f6f4 v[150:153], v[16:23], v[40:47], v[150:153], v226, v228 op_sel_hi:[0,0,0]
	v_mfma_scale_f32_16x16x128_f8f6f4 v[146:149], v[24:31], v[40:47], v[146:149], v226, v228 op_sel_hi:[0,0,0]
	v_mfma_scale_f32_16x16x128_f8f6f4 v[142:145], v[16:23], v[48:55], v[142:145], v226, v228 op_sel_hi:[0,0,0]
	v_mfma_scale_f32_16x16x128_f8f6f4 v[138:141], v[24:31], v[48:55], v[138:141], v226, v228 op_sel_hi:[0,0,0]
	v_mfma_scale_f32_16x16x128_f8f6f4 v[134:137], v[16:23], v[56:63], v[134:137], v226, v228 op_sel_hi:[0,0,0]
	v_mfma_scale_f32_16x16x128_f8f6f4 v[130:133], v[24:31], v[56:63], v[130:133], v226, v228 op_sel_hi:[0,0,0]
	s_setprio 0
	s_barrier
	s_add_u32 s30, s38, s29
	s_addc_u32 s31, s39, 0
	s_add_i32 s29, s40, s78
	s_nop 0
	v_lshl_add_u64 v[212:213], s[30:31], 0, v[204:205]
	s_mov_b32 m0, s29
	s_nop 0
	ds_read_b128 v[32:35], v248 offset:49152
	ds_read_b128 v[40:43], v248 offset:51200
	ds_read_b128 v[36:39], v249 offset:49152
	ds_read_b128 v[44:47], v249 offset:51200
	ds_read_b128 v[48:51], v248 offset:53248
	ds_read_b128 v[56:59], v248 offset:55296
	ds_read_b128 v[52:55], v249 offset:53248
	ds_read_b128 v[60:63], v249 offset:55296
	global_load_lds_dwordx4 v[212:213], off
	s_add_i32 m0, s29, 0x2000
	v_lshl_add_u64 v[212:213], s[30:31], 0, v[206:207]
	s_add_u32 s30, s30, 0x10000
	s_addc_u32 s31, s31, 0
	s_add_i32 s29, s41, s78
	global_load_lds_dwordx4 v[212:213], off
	v_lshl_add_u64 v[212:213], s[30:31], 0, v[204:205]
	s_mov_b32 m0, s29
	s_nop 0
	global_load_lds_dwordx4 v[212:213], off
	s_add_i32 m0, s29, 0x2000
	s_mov_b32 s29, s97
	s_lshl_b64 s[28:29], s[28:29], 7
	v_lshl_add_u64 v[212:213], s[30:31], 0, v[206:207]
	s_add_u32 s28, s34, s28
	s_nop 0
	global_load_lds_dwordx4 v[212:213], off
	s_addc_u32 s29, s35, s29
	s_mov_b32 m0, s81
	s_nop 0
	s_nop 0
	global_load_lds_dwordx4 v194, s[28:29]
	s_mov_b32 m0, s16
	s_nop 0
	global_load_lds_dwordx4 v196, s[28:29]
	s_waitcnt vmcnt(8)
	s_waitcnt lgkmcnt(0)
	s_barrier
	s_setprio 1
	s_waitcnt lgkmcnt(0)
	s_nop 0
	v_mfma_scale_f32_16x16x128_f8f6f4 v[126:129], v[0:7], v[32:39], v[126:129], v226, v228 op_sel_hi:[0,0,0]
	v_mfma_scale_f32_16x16x128_f8f6f4 v[122:125], v[8:15], v[32:39], v[122:125], v226, v228 op_sel_hi:[0,0,0]
	v_mfma_scale_f32_16x16x128_f8f6f4 v[118:121], v[0:7], v[40:47], v[118:121], v226, v228 op_sel_hi:[0,0,0]
	v_mfma_scale_f32_16x16x128_f8f6f4 v[114:117], v[8:15], v[40:47], v[114:117], v226, v228 op_sel_hi:[0,0,0]
	v_mfma_scale_f32_16x16x128_f8f6f4 v[110:113], v[0:7], v[48:55], v[110:113], v226, v228 op_sel_hi:[0,0,0]
	v_mfma_scale_f32_16x16x128_f8f6f4 v[106:109], v[8:15], v[48:55], v[106:109], v226, v228 op_sel_hi:[0,0,0]
	v_mfma_scale_f32_16x16x128_f8f6f4 v[102:105], v[0:7], v[56:63], v[102:105], v226, v228 op_sel_hi:[0,0,0]
	v_mfma_scale_f32_16x16x128_f8f6f4 v[98:101], v[8:15], v[56:63], v[98:101], v226, v228 op_sel_hi:[0,0,0]
	s_setprio 0
	s_setprio 1
	v_mfma_scale_f32_16x16x128_f8f6f4 v[92:95], v[16:23], v[32:39], v[92:95], v226, v228 op_sel_hi:[0,0,0]
	v_mfma_scale_f32_16x16x128_f8f6f4 v[88:91], v[24:31], v[32:39], v[88:91], v226, v228 op_sel_hi:[0,0,0]
	v_mfma_scale_f32_16x16x128_f8f6f4 v[84:87], v[16:23], v[40:47], v[84:87], v226, v228 op_sel_hi:[0,0,0]
	v_mfma_scale_f32_16x16x128_f8f6f4 v[80:83], v[24:31], v[40:47], v[80:83], v226, v228 op_sel_hi:[0,0,0]
	v_mfma_scale_f32_16x16x128_f8f6f4 v[76:79], v[16:23], v[48:55], v[76:79], v226, v228 op_sel_hi:[0,0,0]
	v_mfma_scale_f32_16x16x128_f8f6f4 v[72:75], v[24:31], v[48:55], v[72:75], v226, v228 op_sel_hi:[0,0,0]
	v_mfma_scale_f32_16x16x128_f8f6f4 v[68:71], v[16:23], v[56:63], v[68:71], v226, v228 op_sel_hi:[0,0,0]
	v_mfma_scale_f32_16x16x128_f8f6f4 v[64:67], v[24:31], v[56:63], v[64:67], v226, v228 op_sel_hi:[0,0,0]
	s_setprio 0
	s_barrier
	s_cmp_gt_u32 s13, 5
	s_cbranch_scc1 .LBB0_1507
	s_mov_b32 s13, s15
	s_branch .LBB0_1475

.LBB0_1585:
	v_and_b32_e32 v12, 15, v8
	v_lshrrev_b32_e32 v13, 4, v8
	s_lshl_b32 s19, s19, 5
	v_lshl_or_b32 v86, s20, 6, v12
	v_bfe_u32 v13, v13, 1, 1
	s_lshl_b32 s20, s20, 13
	s_and_b32 s19, s19, 0x60
	s_mov_b64 s[28:29], 0x80
	v_lshl_or_b32 v16, v13, 10, s20
	s_lshr_b32 s20, s19, 3
	s_add_i32 m0, s7, 0x18000
	v_lshl_add_u64 v[6:7], v[6:7], 0, s[28:29]
	v_or_b32_e32 v13, s20, v13
	s_waitcnt vmcnt(2)
	s_barrier
	global_load_lds_dwordx4 v[6:7], off
	v_lshl_add_u64 v[4:5], v[4:5], 0, s[28:29]
	s_add_i32 m0, s7, 0x1a000
	s_add_i32 s20, s7, 0x8000
	s_add_i32 s21, s7, 0xa000
	global_load_lds_dwordx4 v[4:5], off
	v_lshl_add_u64 v[2:3], v[2:3], 0, s[28:29]
	s_mov_b32 m0, s20
	v_lshl_add_u64 v[0:1], v[0:1], 0, s[28:29]
	s_add_u32 s28, s8, 0x10080
	global_load_lds_dwordx4 v[2:3], off
	s_mov_b32 m0, s21
	s_addc_u32 s29, s9, 0
	s_add_i32 s8, s7, 0x1c000
	global_load_lds_dwordx4 v[0:1], off
	v_lshl_add_u64 v[0:1], s[28:29], 0, v[96:97]
	s_mov_b32 m0, s8
	s_add_i32 s9, s7, 0x1e000
	global_load_lds_dwordx4 v[0:1], off
	v_lshl_add_u64 v[0:1], s[28:29], 0, v[72:73]
	s_mov_b32 m0, s9
	s_cmp_lt_u32 s22, 5
	global_load_lds_dwordx4 v[0:1], off
	s_cselect_b32 s23, 1, 2
	s_min_u32 s26, s22, 4
	s_add_i32 s25, s22, 1
	s_add_i32 s26, s26, -1
	s_cmp_lt_i32 s22, 3
	s_cselect_b32 s23, 0, s23
	s_cselect_b32 s25, s25, s26
	s_or_b32 s23, s23, s24
	s_add_i32 s24, s25, s24
	s_add_u32 s4, s59, s4
	s_addc_u32 s5, s60, s5
	s_add_u32 s25, s4, s0
	s_addc_u32 s26, s5, s1
	s_add_u32 s0, s70, 0x2ee00080
	v_lshlrev_b32_e32 v0, 13, v9
	s_addc_u32 s1, s71, 0
	s_add_i32 s4, s27, 0x30000
	v_and_b32_e32 v2, 0xffffc000, v0
	v_lshlrev_b32_e32 v3, 10, v10
	v_and_b32_e32 v1, 1, v9
	v_lshlrev_b32_e32 v14, 1, v8
	v_add3_u32 v0, s4, v2, v3
	v_lshlrev_b32_e32 v4, 6, v1
	v_lshlrev_b32_e32 v5, 1, v11
	v_bfe_u32 v79, v8, 4, 2
	v_and_b32_e32 v14, 32, v14
	v_lshlrev_b32_e32 v12, 6, v12
	v_lshlrev_b32_e32 v8, 2, v8
	v_add3_u32 v0, v0, v4, v5
	v_mov_b32_e32 v1, v97
	s_add_i32 s27, s27, 0x20000
	v_or_b32_e32 v15, v12, v14
	v_and_b32_e32 v8, 32, v8
	v_lshlrev_b32_e32 v13, 10, v13
	v_lshl_add_u64 v[74:75], s[0:1], 0, v[0:1]
	v_add3_u32 v0, s27, v2, v3
	v_bitop3_b32 v12, v12, v8, v14 bitop3:0x36
	v_bitop3_b32 v80, v13, v15, v8 bitop3:0xf6
	v_or_b32_e32 v14, 16, v15
	v_bitop3_b32 v15, v15, v8, 16 bitop3:0x36
	s_waitcnt vmcnt(6)
	v_add3_u32 v0, v0, v4, v5
	v_or_b32_e32 v12, v12, v16
	v_or_b32_e32 v15, v15, v16
	v_lshl_add_u64 v[76:77], s[0:1], 0, v[0:1]
	v_mov_b32_e32 v0, 0
	v_mov_b32_e32 v69, v97
	v_mov_b32_e32 v71, v97
	v_bitop3_b32 v81, v14, v13, v8 bitop3:0xde
	s_mov_b32 s22, 0
	s_mov_b64 s[0:1], 0
	v_add_u32_e32 v82, 0, v12
	v_add_u32_e32 v83, 0, v15
	v_mbcnt_lo_u32_b32 v84, -1, 0
	v_mbcnt_hi_u32_b32 v84, -1, v84
	v_and_b32_e32 v84, 16, v84
	v_xor_b32_e32 v82, v82, v84
	v_xor_b32_e32 v83, v83, v84
	v_xor_b32_e32 v80, v80, v84
	v_xor_b32_e32 v81, v81, v84
	v_mov_b32_e32 v1, v0
	v_mov_b32_e32 v2, v0
	v_mov_b32_e32 v3, v0
	v_mov_b32_e32 v4, v0
	v_mov_b32_e32 v5, v0
	v_mov_b32_e32 v6, v0
	v_mov_b32_e32 v7, v0
	v_mov_b32_e32 v8, v0
	v_mov_b32_e32 v9, v0
	v_mov_b32_e32 v10, v0
	v_mov_b32_e32 v11, v0
	v_mov_b32_e32 v12, v0
	v_mov_b32_e32 v13, v0
	v_mov_b32_e32 v14, v0
	v_mov_b32_e32 v15, v0
	v_mov_b32_e32 v16, v0
	v_mov_b32_e32 v17, v0
	v_mov_b32_e32 v18, v0
	v_mov_b32_e32 v19, v0
	v_mov_b32_e32 v20, v0
	v_mov_b32_e32 v21, v0
	v_mov_b32_e32 v22, v0
	v_mov_b32_e32 v23, v0
	v_mov_b32_e32 v24, v0
	v_mov_b32_e32 v25, v0
	v_mov_b32_e32 v26, v0
	v_mov_b32_e32 v27, v0
	v_mov_b32_e32 v28, v0
	v_mov_b32_e32 v29, v0
	v_mov_b32_e32 v30, v0
	v_mov_b32_e32 v31, v0
	v_mov_b32_e32 v32, v0
	v_mov_b32_e32 v33, v0
	v_mov_b32_e32 v34, v0
	v_mov_b32_e32 v35, v0
	v_mov_b32_e32 v36, v0
	v_mov_b32_e32 v37, v0
	v_mov_b32_e32 v38, v0
	v_mov_b32_e32 v39, v0
	v_mov_b32_e32 v40, v0
	v_mov_b32_e32 v41, v0
	v_mov_b32_e32 v42, v0
	v_mov_b32_e32 v43, v0
	v_mov_b32_e32 v44, v0
	v_mov_b32_e32 v45, v0
	v_mov_b32_e32 v46, v0
	v_mov_b32_e32 v47, v0
	v_mov_b32_e32 v48, v0
	v_mov_b32_e32 v49, v0
	v_mov_b32_e32 v50, v0
	v_mov_b32_e32 v51, v0
	v_mov_b32_e32 v52, v0
	v_mov_b32_e32 v53, v0
	v_mov_b32_e32 v54, v0
	v_mov_b32_e32 v55, v0
	v_mov_b32_e32 v56, v0
	v_mov_b32_e32 v57, v0
	v_mov_b32_e32 v58, v0
	v_mov_b32_e32 v59, v0
	v_mov_b32_e32 v60, v0
	v_mov_b32_e32 v61, v0
	v_mov_b32_e32 v62, v0
	v_mov_b32_e32 v63, v0
	s_barrier
	s_nop 0
.LBB0_1586:
	s_add_i32 s30, 0, 0x10000
	v_add_u32_e32 v84, s30, v80
	v_add_u32_e32 v85, s30, v81
	ds_read_b128 v[88:91], v84
	ds_read_b128 v[92:95], v85
	v_add_u32_e32 v84, s76, v80
	v_add_u32_e32 v85, s76, v81
	ds_read_b128 v[98:101], v84
	ds_read_b128 v[102:105], v85
	v_lshl_add_u64 v[84:85], v[76:77], 0, s[0:1]
	s_add_i32 m0, s7, 0xc000
	ds_read_b128 v[106:109], v82
	ds_read_b128 v[114:117], v82 offset:2048
	ds_read_b128 v[110:113], v83
	ds_read_b128 v[118:121], v83 offset:2048
	ds_read_b128 v[122:125], v82 offset:4096
	ds_read_b128 v[130:133], v82 offset:6144
	ds_read_b128 v[126:129], v83 offset:4096
	ds_read_b128 v[134:137], v83 offset:6144
	global_load_lds_dwordx4 v[84:85], off
	v_lshl_add_u64 v[84:85], v[74:75], 0, s[0:1]
	s_add_i32 m0, s7, 0xe000
	s_nop 0
	s_nop 0
	global_load_lds_dwordx4 v[84:85], off
	s_waitcnt vmcnt(8)
	s_waitcnt lgkmcnt(0)
	s_barrier
	s_setprio 1
	s_waitcnt lgkmcnt(0)
	s_nop 0
	v_mfma_scale_f32_16x16x128_f8f6f4 v[138:141], v[88:95], v[106:113], v[60:63], v226, v228 op_sel_hi:[0,0,0]
	v_mfma_scale_f32_16x16x128_f8f6f4 v[106:109], v[98:105], v[106:113], v[56:59], v226, v228 op_sel_hi:[0,0,0]
	v_mfma_scale_f32_16x16x128_f8f6f4 v[110:113], v[88:95], v[114:121], v[52:55], v226, v228 op_sel_hi:[0,0,0]
	v_mfma_scale_f32_16x16x128_f8f6f4 v[114:117], v[98:105], v[114:121], v[48:51], v226, v228 op_sel_hi:[0,0,0]
	v_mfma_scale_f32_16x16x128_f8f6f4 v[118:121], v[88:95], v[122:129], v[44:47], v226, v228 op_sel_hi:[0,0,0]
	v_mfma_scale_f32_16x16x128_f8f6f4 v[122:125], v[98:105], v[122:129], v[40:43], v226, v228 op_sel_hi:[0,0,0]
	v_mfma_scale_f32_16x16x128_f8f6f4 v[126:129], v[88:95], v[130:137], v[36:39], v226, v228 op_sel_hi:[0,0,0]
	v_mfma_scale_f32_16x16x128_f8f6f4 v[130:133], v[98:105], v[130:137], v[32:35], v226, v228 op_sel_hi:[0,0,0]
	s_setprio 0
	s_barrier
	s_add_i32 s27, s22, 2
	s_cmpk_lg_i32 s0, 0x300
	s_cselect_b32 s96, s27, 0
	s_cmp_lt_u32 s96, 4
	s_cselect_b32 s4, s23, s24
	s_ashr_i32 s5, s4, 31
	s_lshl_b64 s[28:29], s[4:5], 19
	s_lshl_b32 s4, s96, 7
	s_and_b32 s5, s4, 0x100
	s_or_b32 s4, s96, 1
	s_lshl_b32 s31, s4, 7
	s_and_b32 s31, s31, 0x180
	s_add_u32 s38, s25, s28
	s_addc_u32 s39, s26, s29
	s_add_u32 s28, s38, s5
	s_addc_u32 s29, s39, 0
	s_add_i32 s5, s30, s14
	s_nop 0
	v_lshl_add_u64 v[84:85], s[28:29], 0, v[96:97]
	s_mov_b32 m0, s5
	s_nop 0
	ds_read_b128 v[32:35], v82 offset:16384
	ds_read_b128 v[40:43], v82 offset:18432
	ds_read_b128 v[36:39], v83 offset:16384
	ds_read_b128 v[44:47], v83 offset:18432
	ds_read_b128 v[48:51], v82 offset:20480
	ds_read_b128 v[56:59], v82 offset:22528
	ds_read_b128 v[52:55], v83 offset:20480
	ds_read_b128 v[60:63], v83 offset:22528
	global_load_lds_dwordx4 v[84:85], off
	s_add_i32 m0, s5, 0x2000
	v_lshl_add_u64 v[84:85], s[28:29], 0, v[72:73]
	s_add_u32 s28, s28, 0x10000
	s_addc_u32 s29, s29, 0
	s_nop 0
	global_load_lds_dwordx4 v[84:85], off
	v_lshl_add_u64 v[84:85], s[28:29], 0, v[96:97]
	s_mov_b32 m0, s11
	s_nop 0
	global_load_lds_dwordx4 v[84:85], off
	v_lshl_add_u64 v[84:85], s[28:29], 0, v[72:73]
	s_lshl_b64 s[28:29], s[96:97], 7
	s_add_u32 s28, s34, s28
	s_mov_b32 m0, s15
	s_addc_u32 s29, s35, s29
	global_load_lds_dwordx4 v[84:85], off
	v_lshl_add_u64 v[84:85], s[28:29], 0, v[64:65]
	s_mov_b32 m0, s7
	s_nop 0
	global_load_lds_dwordx4 v[84:85], off
	v_lshl_add_u64 v[84:85], s[28:29], 0, v[66:67]
	s_mov_b32 m0, s16
	s_nop 0
	global_load_lds_dwordx4 v[84:85], off
	s_waitcnt vmcnt(8)
	s_waitcnt lgkmcnt(0)
	s_barrier
	s_setprio 1
	s_waitcnt lgkmcnt(0)
	s_nop 0
	v_mfma_scale_f32_16x16x128_f8f6f4 v[134:137], v[88:95], v[32:39], v[28:31], v226, v228 op_sel_hi:[0,0,0]
	v_mfma_scale_f32_16x16x128_f8f6f4 v[142:145], v[98:105], v[32:39], v[24:27], v226, v228 op_sel_hi:[0,0,0]
	v_mfma_scale_f32_16x16x128_f8f6f4 v[146:149], v[88:95], v[40:47], v[20:23], v226, v228 op_sel_hi:[0,0,0]
	v_mfma_scale_f32_16x16x128_f8f6f4 v[150:153], v[98:105], v[40:47], v[16:19], v226, v228 op_sel_hi:[0,0,0]
	v_mfma_scale_f32_16x16x128_f8f6f4 v[154:157], v[88:95], v[48:55], v[12:15], v226, v228 op_sel_hi:[0,0,0]
	v_mfma_scale_f32_16x16x128_f8f6f4 v[158:161], v[98:105], v[48:55], v[8:11], v226, v228 op_sel_hi:[0,0,0]
	v_mfma_scale_f32_16x16x128_f8f6f4 v[162:165], v[88:95], v[56:63], v[4:7], v226, v228 op_sel_hi:[0,0,0]
	v_mfma_scale_f32_16x16x128_f8f6f4 v[166:169], v[98:105], v[56:63], v[0:3], v226, v228 op_sel_hi:[0,0,0]
	s_setprio 0
	s_barrier
	s_add_i32 s5, 0, 0x18000
	s_nop 3
	v_add_u32_e32 v0, s5, v80
	v_add_u32_e32 v4, s5, v81
	v_add_u32_e32 v8, s94, v80
	ds_read_b128 v[0:3], v0
	ds_read_b128 v[4:7], v4
	v_add_u32_e64 v9, s94, v81
	ds_read_b128 v[88:91], v8
	ds_read_b128 v[92:95], v9
	s_mov_b32 m0, s17
	s_nop 0
	v_lshl_add_u64 v[32:33], s[28:29], 0, v[68:69]
	ds_read_b128 v[8:11], v82 offset:32768
	ds_read_b128 v[16:19], v82 offset:34816
	ds_read_b128 v[12:15], v83 offset:32768
	ds_read_b128 v[20:23], v83 offset:34816
	ds_read_b128 v[24:27], v82 offset:36864
	ds_read_b128 v[98:101], v82 offset:38912
	ds_read_b128 v[28:31], v83 offset:36864
	ds_read_b128 v[102:105], v83 offset:38912
	global_load_lds_dwordx4 v[32:33], off
	v_lshl_add_u64 v[32:33], s[28:29], 0, v[70:71]
	s_mov_b32 m0, s18
	s_nop 0
	global_load_lds_dwordx4 v[32:33], off
	s_waitcnt vmcnt(8)
	s_waitcnt lgkmcnt(0)
	s_barrier
	s_setprio 1
	s_waitcnt lgkmcnt(0)
	s_nop 0
	v_mfma_scale_f32_16x16x128_f8f6f4 v[60:63], v[0:7], v[8:15], v[138:141], v226, v228 op_sel_hi:[0,0,0]
	v_mfma_scale_f32_16x16x128_f8f6f4 v[56:59], v[88:95], v[8:15], v[106:109], v226, v228 op_sel_hi:[0,0,0]
	v_mfma_scale_f32_16x16x128_f8f6f4 v[52:55], v[0:7], v[16:23], v[110:113], v226, v228 op_sel_hi:[0,0,0]
	v_mfma_scale_f32_16x16x128_f8f6f4 v[48:51], v[88:95], v[16:23], v[114:117], v226, v228 op_sel_hi:[0,0,0]
	v_mfma_scale_f32_16x16x128_f8f6f4 v[44:47], v[0:7], v[24:31], v[118:121], v226, v228 op_sel_hi:[0,0,0]
	v_mfma_scale_f32_16x16x128_f8f6f4 v[40:43], v[88:95], v[24:31], v[122:125], v226, v228 op_sel_hi:[0,0,0]
	v_mfma_scale_f32_16x16x128_f8f6f4 v[36:39], v[0:7], v[98:105], v[126:129], v226, v228 op_sel_hi:[0,0,0]
	v_mfma_scale_f32_16x16x128_f8f6f4 v[32:35], v[88:95], v[98:105], v[130:133], v226, v228 op_sel_hi:[0,0,0]
	s_setprio 0
	s_barrier
	s_add_u32 s28, s38, s31
	s_addc_u32 s29, s39, 0
	s_add_i32 s5, s5, s14
	s_nop 0
	v_lshl_add_u64 v[16:17], s[28:29], 0, v[96:97]
	s_mov_b32 m0, s5
	s_nop 0
	ds_read_b128 v[8:11], v82 offset:49152
	ds_read_b128 v[98:101], v82 offset:51200
	ds_read_b128 v[12:15], v83 offset:49152
	ds_read_b128 v[102:105], v83 offset:51200
	ds_read_b128 v[106:109], v82 offset:53248
	ds_read_b128 v[114:117], v82 offset:55296
	ds_read_b128 v[110:113], v83 offset:53248
	ds_read_b128 v[118:121], v83 offset:55296
	global_load_lds_dwordx4 v[16:17], off
	s_add_i32 m0, s5, 0x2000
	v_lshl_add_u64 v[16:17], s[28:29], 0, v[72:73]
	s_add_u32 s28, s28, 0x10000
	s_mov_b32 s5, s97
	s_addc_u32 s29, s29, 0
	s_lshl_b64 s[4:5], s[4:5], 7
	s_nop 0
	global_load_lds_dwordx4 v[16:17], off
	v_lshl_add_u64 v[16:17], s[28:29], 0, v[96:97]
	s_mov_b32 m0, s8
	s_add_u32 s4, s34, s4
	global_load_lds_dwordx4 v[16:17], off
	v_lshl_add_u64 v[16:17], s[28:29], 0, v[72:73]
	s_mov_b32 m0, s9
	s_addc_u32 s5, s35, s5
	global_load_lds_dwordx4 v[16:17], off
	v_lshl_add_u64 v[16:17], s[4:5], 0, v[64:65]
	s_mov_b32 m0, s20
	s_nop 0
	global_load_lds_dwordx4 v[16:17], off
	v_lshl_add_u64 v[16:17], s[4:5], 0, v[66:67]
	s_mov_b32 m0, s21
	s_nop 0
	global_load_lds_dwordx4 v[16:17], off
	s_waitcnt vmcnt(8)
	s_waitcnt lgkmcnt(0)
	s_barrier
	s_setprio 1
	s_waitcnt lgkmcnt(0)
	s_nop 0
	v_mfma_scale_f32_16x16x128_f8f6f4 v[28:31], v[0:7], v[8:15], v[134:137], v226, v228 op_sel_hi:[0,0,0]
	v_mfma_scale_f32_16x16x128_f8f6f4 v[24:27], v[88:95], v[8:15], v[142:145], v226, v228 op_sel_hi:[0,0,0]
	v_mfma_scale_f32_16x16x128_f8f6f4 v[20:23], v[0:7], v[98:105], v[146:149], v226, v228 op_sel_hi:[0,0,0]
	v_mfma_scale_f32_16x16x128_f8f6f4 v[16:19], v[88:95], v[98:105], v[150:153], v226, v228 op_sel_hi:[0,0,0]
	v_mfma_scale_f32_16x16x128_f8f6f4 v[12:15], v[0:7], v[106:113], v[154:157], v226, v228 op_sel_hi:[0,0,0]
	v_mfma_scale_f32_16x16x128_f8f6f4 v[8:11], v[88:95], v[106:113], v[158:161], v226, v228 op_sel_hi:[0,0,0]
	v_mfma_scale_f32_16x16x128_f8f6f4 v[4:7], v[0:7], v[114:121], v[162:165], v226, v228 op_sel_hi:[0,0,0]
	v_mfma_scale_f32_16x16x128_f8f6f4 v[0:3], v[88:95], v[114:121], v[166:169], v226, v228 op_sel_hi:[0,0,0]
	s_setprio 0
	s_barrier
	s_add_u32 s0, s0, 0x100
	s_addc_u32 s1, s1, 0
	s_cmp_gt_u32 s22, 5
	s_mov_b32 s22, s27
	s_cbranch_scc0 .LBB0_1586
	s_cmpk_lt_u32 s13, 0x100
	s_cbranch_scc0 .LBB0_1589
	s_barrier
